# v29 + non-temporal hint on the scan chains' read-once chunk-operand loads
# speedup vs baseline: 1.0628x; 1.0028x over previous
.Lscan_nomap:
	s_cmpk_lt_i32 s91, 0xa0
	s_cbranch_scc1 .LBB0_1526
	s_cmp_gt_i32 s18, 31
	s_cbranch_scc0 .LBB0_1369
	s_cmpk_gt_u32 s18, 0x5f
	s_cbranch_scc0 .LBB0_1370
	s_cmpk_gt_u32 s18, 0x7f
	s_cbranch_scc0 .LBB0_1371
	s_mov_b64 s[4:5], 0
	s_cmpk_lt_u32 s18, 0xc0
	s_mov_b64 s[6:7], 0
	s_cbranch_scc0 .LBB0_1372
	s_add_i32 s9, s18, 0xffffff80
	v_ashrrev_i32_e32 v229, 4, v228
	s_lshl_b32 s7, s9, 8
	v_lshlrev_b32_e32 v158, 6, v229
	s_lshl_b32 s6, s9, 6
	s_and_b32 s34, s7, 0x3800
	v_ashrrev_i32_e32 v159, 31, v158
	s_and_b32 s6, s6, 0x1c0
	v_and_b32_e32 v161, 15, v227
	v_lshl_add_u64 v[172:173], s[34:35], 0, v[158:159]
	v_lshl_or_b32 v160, v161, 2, s6
	s_waitcnt vmcnt(0)
	v_lshlrev_b64 v[0:1], 11, v[172:173]
	s_waitcnt lgkmcnt(0)
	v_lshl_add_u64 v[0:1], s[48:49], 0, v[0:1]
	v_lshlrev_b32_e32 v32, 2, v160
	v_mov_b32_e32 v33, v65
	v_lshl_add_u64 v[16:17], v[0:1], 0, v[32:33]
	s_mov_b64 s[6:7], 0x6e200000
	v_lshl_add_u64 v[4:5], v[16:17], 0, s[6:7]
	v_lshlrev_b64 v[0:1], 10, v[172:173]
	s_mov_b32 s6, 0x6e201000
	v_lshl_add_u64 v[0:1], s[48:49], 0, v[0:1]
	v_lshlrev_b32_e32 v64, 1, v160
	v_add_co_u32_e32 v12, vcc, s6, v16
	v_lshl_add_u64 v[34:35], v[0:1], 0, v[64:65]
	s_nop 0
	v_addc_co_u32_e32 v13, vcc, 0, v17, vcc
	s_mov_b32 s6, 0x70201000
	v_add_co_u32_e32 v36, vcc, s6, v34
	s_mov_b32 s6, 0x6e202000
	s_nop 0
	v_addc_co_u32_e32 v37, vcc, 0, v35, vcc
	v_add_co_u32_e32 v20, vcc, s6, v16
	s_mov_b32 s6, 0x6e203000
	s_nop 0
	v_addc_co_u32_e32 v21, vcc, 0, v17, vcc
	v_add_co_u32_e32 v28, vcc, s6, v16
	s_mov_b64 s[6:7], 0x70200000
	global_load_dwordx4 v[0:3], v[12:13], off offset:-4096 nt
	s_nop 0
	global_load_dwordx4 v[4:7], v[4:5], off offset:2048 nt
	s_nop 0
	global_load_dwordx4 v[8:11], v[12:13], off nt
	s_nop 0
	global_load_dwordx4 v[12:15], v[12:13], off offset:2048 nt
	v_addc_co_u32_e32 v29, vcc, 0, v17, vcc
	v_lshl_add_u64 v[34:35], v[34:35], 0, s[6:7]
	global_load_dwordx4 v[16:19], v[28:29], off offset:-4096 nt
	s_nop 0
	global_load_dwordx4 v[20:23], v[20:21], off offset:2048 nt
	s_nop 0
	global_load_dwordx4 v[24:27], v[28:29], off nt
	s_nop 0
	global_load_dwordx4 v[28:31], v[28:29], off offset:2048 nt
	s_nop 0
	global_load_dwordx2 v[138:139], v[36:37], off offset:-4096 nt
	global_load_dwordx2 v[140:141], v[34:35], off offset:1024 nt
	global_load_dwordx2 v[142:143], v[34:35], off offset:2048 nt
	global_load_dwordx2 v[144:145], v[34:35], off offset:3072 nt
	global_load_dwordx2 v[148:149], v[36:37], off nt
	global_load_dwordx2 v[152:153], v[36:37], off offset:1024 nt
	global_load_dwordx2 v[154:155], v[36:37], off offset:2048 nt
	global_load_dwordx2 v[156:157], v[36:37], off offset:3072 nt
	s_lshl_b32 s6, s9, 19
	s_lshl_b32 s7, s9, 18
	s_and_b32 s34, s6, 0x1c00000
	v_lshlrev_b64 v[34:35], 11, v[158:159]
	v_lshlrev_b64 v[36:37], 10, v[158:159]
	v_lshl_add_u64 v[146:147], s[34:35], 0, v[34:35]
	s_and_b32 s34, s7, 0xe00000
	v_lshl_add_u64 v[150:151], s[34:35], 0, v[36:37]
	v_mov_b32_e32 v48, 0
	v_mov_b32_e32 v52, 1.0
	v_or_b32_e32 v146, v146, v32
	v_or_b32_e32 v150, v150, v64
	s_mov_b32 s8, 0
	s_bfe_u32 s12, s9, 0x30003
	v_mov_b32_e32 v53, v52
	v_mov_b32_e32 v54, v52
	v_mov_b32_e32 v55, v52
	v_mov_b32_e32 v49, v48
	v_mov_b32_e32 v50, v48
	v_mov_b32_e32 v51, v48
	v_mov_b64_e32 v[174:175], v[146:147]
	v_mov_b64_e32 v[176:177], v[150:151]
	s_waitcnt vmcnt(14)
	v_mov_b64_e32 v[112:113], v[6:7]
	v_mov_b64_e32 v[120:121], v[2:3]
	s_waitcnt vmcnt(13)
	v_mov_b64_e32 v[100:101], v[10:11]
	s_waitcnt vmcnt(12)
	v_mov_b64_e32 v[96:97], v[14:15]
	s_waitcnt vmcnt(11)
	v_mov_b64_e32 v[88:89], v[18:19]
	s_waitcnt vmcnt(10)
	v_mov_b64_e32 v[84:85], v[22:23]
	s_waitcnt vmcnt(9)
	v_mov_b64_e32 v[80:81], v[26:27]
	s_waitcnt vmcnt(8)
	v_mov_b64_e32 v[76:77], v[30:31]
	v_mov_b64_e32 v[34:35], v[2:3]
	v_mov_b64_e32 v[38:39], v[6:7]
	v_mov_b64_e32 v[42:43], v[10:11]
	v_mov_b64_e32 v[46:47], v[14:15]
	v_mov_b64_e32 v[58:59], v[18:19]
	v_mov_b64_e32 v[62:63], v[22:23]
	v_mov_b64_e32 v[68:69], v[26:27]
	v_mov_b64_e32 v[72:73], v[30:31]
	v_mov_b64_e32 v[118:119], v[0:1]
	v_mov_b64_e32 v[110:111], v[4:5]
	v_mov_b64_e32 v[98:99], v[8:9]
	v_mov_b64_e32 v[94:95], v[12:13]
	v_mov_b64_e32 v[86:87], v[16:17]
	v_mov_b64_e32 v[82:83], v[20:21]
	v_mov_b64_e32 v[78:79], v[24:25]
	v_mov_b64_e32 v[74:75], v[28:29]
	s_waitcnt vmcnt(7)
	v_mov_b32_e32 v244, v138
	v_mov_b32_e32 v245, v139
	s_waitcnt vmcnt(6)
	v_mov_b32_e32 v242, v140
	v_mov_b32_e32 v243, v141
	s_waitcnt vmcnt(5)
	v_mov_b32_e32 v240, v142
	v_mov_b32_e32 v241, v143
	s_waitcnt vmcnt(4)
	v_mov_b32_e32 v238, v144
	v_mov_b32_e32 v239, v145
	s_waitcnt vmcnt(3)
	v_mov_b32_e32 v236, v148
	v_mov_b32_e32 v237, v149
	s_waitcnt vmcnt(2)
	v_mov_b32_e32 v234, v152
	v_mov_b32_e32 v235, v153
	s_waitcnt vmcnt(1)
	v_mov_b32_e32 v232, v154
	v_mov_b32_e32 v233, v155
	s_waitcnt vmcnt(0)
	v_mov_b32_e32 v230, v156
	v_mov_b32_e32 v231, v157
	v_mov_b64_e32 v[32:33], v[0:1]
	v_mov_b64_e32 v[36:37], v[4:5]
	v_mov_b64_e32 v[40:41], v[8:9]
	v_mov_b64_e32 v[44:45], v[12:13]
	v_mov_b64_e32 v[56:57], v[16:17]
	v_mov_b64_e32 v[60:61], v[20:21]
	v_mov_b64_e32 v[66:67], v[24:25]
	v_mov_b64_e32 v[70:71], v[28:29]
	s_branch .LBB0_1367

.LBB0_1367:
	v_lshl_add_u64 v[210:211], s[48:49], 0, v[174:175]
	s_mov_b32 s6, 0x6e204000
	v_add_co_u32_e32 v90, vcc, s6, v210
	s_mov_b32 s6, 0x6e205000
	s_nop 0
	v_addc_co_u32_e32 v91, vcc, 0, v211, vcc
	v_add_co_u32_e32 v92, vcc, s6, v210
	v_lshl_add_u64 v[212:213], s[48:49], 0, v[176:177]
	s_nop 0
	v_addc_co_u32_e32 v93, vcc, 0, v211, vcc
	s_mov_b32 s6, 0x70202000
	v_add_co_u32_e32 v102, vcc, s6, v212
	s_mov_b32 s6, 0x70203000
	s_nop 0
	v_addc_co_u32_e32 v103, vcc, 0, v213, vcc
	v_add_co_u32_e32 v162, vcc, s6, v212
	s_mov_b32 s6, 0x6e206000
	s_nop 0
	v_addc_co_u32_e32 v163, vcc, 0, v213, vcc
	global_load_dwordx4 v[130:133], v[90:91], off offset:2048 nt
	global_load_dwordx2 v[206:207], v[102:103], off offset:1024 nt
	global_load_dwordx4 v[134:137], v[92:93], off offset:-4096 nt
	global_load_dwordx4 v[126:129], v[92:93], off nt
	global_load_dwordx2 v[208:209], v[162:163], off offset:-4096 nt
	global_load_dwordx4 v[122:125], v[92:93], off offset:2048 nt
	global_load_dwordx2 v[204:205], v[102:103], off offset:2048 nt
	global_load_dwordx2 v[192:193], v[102:103], off offset:3072 nt
	v_add_co_u32_e32 v90, vcc, s6, v210
	s_cmp_gt_u32 s8, 47
	s_nop 0
	v_addc_co_u32_e32 v91, vcc, 0, v211, vcc
	global_load_dwordx4 v[114:117], v[90:91], off nt
	global_load_dwordx4 v[106:109], v[90:91], off offset:2048 nt
	v_add_co_u32_e32 v90, vcc, 0x6e207000, v210
	s_cselect_b64 s[6:7], -1, 0
	s_nop 0
	v_addc_co_u32_e32 v91, vcc, 0, v211, vcc
	global_load_dwordx4 v[102:105], v[90:91], off nt
	s_nop 0
	global_load_dwordx4 v[90:93], v[90:91], off offset:2048 nt
	s_nop 0
	global_load_dwordx2 v[196:197], v[162:163], off nt
	global_load_dwordx2 v[190:191], v[162:163], off offset:1024 nt
	global_load_dwordx2 v[188:189], v[162:163], off offset:2048 nt
	global_load_dwordx2 v[180:181], v[162:163], off offset:3072 nt
	s_cmp_lt_u32 s8, 48
	v_mov_b32_e32 v178, v244
	v_mov_b32_e32 v179, v245
	v_mov_b32_e32 v182, v242
	v_mov_b32_e32 v183, v243
	v_mov_b32_e32 v184, v240
	v_mov_b32_e32 v185, v241
	v_mov_b32_e32 v186, v238
	v_mov_b32_e32 v187, v239
	v_mov_b32_e32 v194, v236
	v_mov_b32_e32 v195, v237
	v_mov_b32_e32 v198, v234
	v_mov_b32_e32 v199, v235
	v_mov_b32_e32 v200, v232
	v_mov_b32_e32 v201, v233
	v_mov_b32_e32 v202, v230
	v_mov_b32_e32 v203, v231
	s_cbranch_scc0 .LBB0_1366
	v_add_co_u32_e32 v36, vcc, 0x6e208000, v210
	s_nop 1
	v_addc_co_u32_e32 v37, vcc, 0, v211, vcc
	v_add_co_u32_e32 v56, vcc, 0x70204000, v212
	global_load_dwordx4 v[32:35], v[36:37], off nt
	s_nop 0
	global_load_dwordx4 v[36:39], v[36:37], off offset:2048 nt
	v_addc_co_u32_e32 v57, vcc, 0, v213, vcc
	v_add_co_u32_e32 v44, vcc, 0x6e209000, v210
	s_nop 1
	v_addc_co_u32_e32 v45, vcc, 0, v211, vcc
	v_add_co_u32_e32 v60, vcc, 0x6e20a000, v210
	global_load_dwordx4 v[40:43], v[44:45], off nt
	s_nop 0
	global_load_dwordx4 v[44:47], v[44:45], off offset:2048 nt
	s_nop 0
	global_load_dwordx2 v[178:179], v[56:57], off nt
	global_load_dwordx2 v[182:183], v[56:57], off offset:1024 nt
	global_load_dwordx2 v[184:185], v[56:57], off offset:2048 nt
	global_load_dwordx2 v[186:187], v[56:57], off offset:3072 nt
	v_addc_co_u32_e32 v61, vcc, 0, v211, vcc
	v_add_co_u32_e32 v162, vcc, 0x70205000, v212
	global_load_dwordx4 v[56:59], v[60:61], off nt
	s_nop 0
	global_load_dwordx4 v[60:63], v[60:61], off offset:2048 nt
	v_addc_co_u32_e32 v163, vcc, 0, v213, vcc
	v_add_co_u32_e32 v70, vcc, 0x6e20b000, v210
	s_nop 1
	v_addc_co_u32_e32 v71, vcc, 0, v211, vcc
	global_load_dwordx4 v[66:69], v[70:71], off nt
	s_nop 0
	global_load_dwordx4 v[70:73], v[70:71], off offset:2048 nt
	s_nop 0
	global_load_dwordx2 v[194:195], v[162:163], off nt
	global_load_dwordx2 v[198:199], v[162:163], off offset:1024 nt
	global_load_dwordx2 v[200:201], v[162:163], off offset:2048 nt
	global_load_dwordx2 v[202:203], v[162:163], off offset:3072 nt
	s_branch .LBB0_1366

.LBB0_1373:
	s_lshl_b32 s12, s18, 1
	s_ashr_i32 s15, s82, 2
	s_add_i32 s16, s15, s12
	s_addk_i32 s16, 0xff40
	s_mul_i32 s5, s16, 0x164000
	s_mul_hi_i32 s4, s16, 0x164000
	s_waitcnt lgkmcnt(0)
	s_add_u32 s5, s48, s5
	s_addc_u32 s6, s49, s4
	s_add_u32 s4, s5, 0xa9600000
	s_addc_u32 s5, s6, 0
	s_and_b32 s13, s82, 3
	s_lshl_b32 s14, s13, 10
	s_add_u32 s6, s4, s14
	v_lshlrev_b32_e32 v106, 4, v227
	s_addc_u32 s7, s5, 0
	v_ashrrev_i32_e32 v107, 31, v106
	v_lshl_add_u64 v[48:49], s[6:7], 0, v[106:107]
	s_waitcnt vmcnt(0)
	v_add_co_u32_e32 v0, vcc, 0x1000, v48
	s_cmp_lt_u32 s13, 2
	s_nop 0
	v_addc_co_u32_e32 v1, vcc, 0, v49, vcc
	global_load_dwordx4 v[8:11], v[48:49], off nt
	global_load_dwordx4 v[12:15], v[0:1], off nt
	v_add_co_u32_e32 v0, vcc, 0x2000, v48
	s_cselect_b64 s[8:9], -1, 0
	s_nop 0
	v_addc_co_u32_e32 v1, vcc, 0, v49, vcc
	v_add_co_u32_e32 v2, vcc, 0x3000, v48
	s_cmp_gt_u32 s13, 1
	s_nop 0
	v_addc_co_u32_e32 v3, vcc, 0, v49, vcc
	global_load_dwordx4 v[20:23], v[0:1], off nt
	global_load_dwordx4 v[16:19], v[2:3], off nt
	s_cbranch_scc1 .LBB0_1375
	v_add_co_u32_e32 v0, vcc, 0x4000, v48
	s_nop 1
	v_addc_co_u32_e32 v1, vcc, 0, v49, vcc
	global_load_dwordx4 v[0:3], v[0:1], off nt
.LBB0_1375:
	s_cmp_eq_u32 s13, 3
	s_cselect_b64 s[6:7], -1, 0
	v_cmp_gt_i32_e32 vcc, 16, v227
	s_and_b64 s[6:7], vcc, s[6:7]
	v_lshl_add_u64 v[50:51], s[4:5], 0, v[106:107]
	s_and_saveexec_b64 s[10:11], s[6:7]
	s_cbranch_execz .LBB0_1377
	v_add_co_u32_e32 v4, vcc, 0x5000, v50
	s_nop 1
	v_addc_co_u32_e32 v5, vcc, 0, v51, vcc
	global_load_dwordx4 v[4:7], v[4:5], off offset:2048 nt

.LBB0_1379:
	s_and_saveexec_b64 s[8:9], s[6:7]
	ds_write_b128 v118, v[4:7] offset:18432
	s_or_b64 exec, exec, s[8:9]
	s_add_u32 s8, s4, s14
	s_addc_u32 s9, s5, 0
	s_add_u32 s8, s8, 0x5900
	s_addc_u32 s9, s9, 0
	v_lshl_add_u64 v[52:53], s[8:9], 0, v[106:107]
	v_add_co_u32_e32 v12, vcc, 0x1000, v52
	s_nop 1
	v_addc_co_u32_e32 v13, vcc, 0, v53, vcc
	v_add_co_u32_e32 v16, vcc, 0x2000, v52
	global_load_dwordx4 v[8:11], v[52:53], off nt
	s_nop 0
	global_load_dwordx4 v[12:15], v[12:13], off nt
	v_addc_co_u32_e32 v17, vcc, 0, v53, vcc
	v_add_co_u32_e32 v18, vcc, 0x3000, v52
	s_nop 1
	v_addc_co_u32_e32 v19, vcc, 0, v53, vcc
	global_load_dwordx4 v[20:23], v[16:17], off nt
	s_nop 0
	global_load_dwordx4 v[16:19], v[18:19], off nt
	s_and_b64 vcc, exec, s[38:39]
	s_cbranch_vccnz .LBB0_1383
	v_add_co_u32_e32 v0, vcc, 0x4000, v52
	s_nop 1
	v_addc_co_u32_e32 v1, vcc, 0, v53, vcc
	global_load_dwordx4 v[0:3], v[0:1], off nt
.LBB0_1383:
	s_and_saveexec_b64 s[8:9], s[6:7]
	s_cbranch_execz .LBB0_1385
	v_add_co_u32_e32 v4, vcc, 0xb000, v50
	s_nop 1
	v_addc_co_u32_e32 v5, vcc, 0, v51, vcc
	global_load_dwordx4 v[4:7], v[4:5], off offset:256 nt
.LBB0_1385:
	s_or_b64 exec, exec, s[8:9]
	s_add_u32 s8, s4, s14
	s_addc_u32 s9, s5, 0
	s_add_u32 s8, s8, 0xb200
	s_addc_u32 s9, s9, 0
	v_lshl_add_u64 v[40:41], s[8:9], 0, v[106:107]
	v_add_co_u32_e32 v24, vcc, 0x1000, v40
	s_nop 1
	v_addc_co_u32_e32 v25, vcc, 0, v41, vcc
	global_load_dwordx4 v[28:31], v[40:41], off nt
	global_load_dwordx4 v[32:35], v[24:25], off nt
	v_add_co_u32_e32 v24, vcc, 0x2000, v40
	s_nop 1
	v_addc_co_u32_e32 v25, vcc, 0, v41, vcc
	v_add_co_u32_e32 v26, vcc, 0x3000, v40
	s_nop 1
	v_addc_co_u32_e32 v27, vcc, 0, v41, vcc
	global_load_dwordx4 v[44:47], v[24:25], off nt
	s_nop 0
	global_load_dwordx4 v[24:27], v[26:27], off nt
	s_and_b64 vcc, exec, s[38:39]
	s_cbranch_vccnz .LBB0_1387
	v_add_co_u32_e32 v36, vcc, 0x4000, v40
	s_nop 1
	v_addc_co_u32_e32 v37, vcc, 0, v41, vcc
	global_load_dwordx4 v[36:39], v[36:37], off nt
.LBB0_1387:
	s_and_saveexec_b64 s[8:9], s[6:7]
	s_cbranch_execz .LBB0_1389
	v_add_co_u32_e32 v40, vcc, 0x10000, v50
	s_nop 1
	v_addc_co_u32_e32 v41, vcc, 0, v51, vcc
	global_load_dwordx4 v[40:43], v[40:41], off offset:2560 nt
.LBB0_1389:
	s_or_b64 exec, exec, s[8:9]
	v_add_co_u32_e32 v48, vcc, 0x4000, v48
	s_lshr_b32 s10, s82, 2
	s_nop 0
	v_addc_co_u32_e32 v49, vcc, 0, v49, vcc
	v_add_co_u32_e32 v50, vcc, 0x4000, v52
	s_ashr_i32 s8, s16, 3
	s_nop 0
	v_addc_co_u32_e32 v51, vcc, 0, v53, vcc
	global_load_dwordx4 v[56:59], v[48:49], off offset:2048 nt
	s_nop 0
	global_load_dwordx4 v[48:51], v[50:51], off offset:2048 nt
	s_add_i32 s12, s12, s10
	s_ashr_i32 s9, s8, 31
	s_and_b32 s10, s12, 7
	s_lshl_b64 s[8:9], s[8:9], 21
	s_lshl_b32 s10, s10, 7
	s_or_b32 s8, s8, s10
	s_lshl_b32 s10, s13, 5
	s_add_i32 s16, s14, 0x4800
	s_or_b32 s8, s8, s10
	v_and_b32_e32 v60, 15, v227
	v_lshlrev_b32_e32 v61, 7, v227
	s_movk_i32 s10, 0xf800
	s_add_u32 s8, s48, s8
	v_and_or_b32 v64, v61, s10, v60
	s_addc_u32 s9, s49, s9
	v_lshl_add_u64 v[60:61], v[64:65], 1, s[8:9]
	s_mov_b64 s[10:11], 0x72200800
	s_add_u32 s8, s8, 0x72200000
	v_lshl_add_u64 v[108:109], v[60:61], 0, s[10:11]
	v_add_u32_e32 v60, 0x2600, v64
	v_mov_b32_e32 v61, v65
	s_addc_u32 s9, s9, 0
	v_lshl_add_u64 v[110:111], v[60:61], 1, s[8:9]
	v_add_u32_e32 v60, 0x2400, v64
	v_lshl_add_u64 v[112:113], v[60:61], 1, s[8:9]
	v_add_u32_e32 v60, 0x2000, v64
	v_mov_b32_e32 v52, v65
	v_lshl_add_u64 v[114:115], v[60:61], 1, s[8:9]
	v_add_u32_e32 v64, 0x2200, v64
	v_mov_b32_e32 v60, 0
	s_waitcnt vmcnt(0) lgkmcnt(0)
	s_barrier
	v_and_b32_e32 v119, -16, v227
	v_mov_b32_e32 v53, v52
	v_mov_b32_e32 v54, v52
	v_mov_b32_e32 v55, v52
	s_mov_b32 s17, 1
	v_lshl_add_u64 v[116:117], v[64:65], 1, s[8:9]
	s_mov_b64 s[8:9], 0
	v_mov_b32_e32 v61, v60
	v_mov_b32_e32 v62, v60
	v_mov_b32_e32 v63, v60
	v_mov_b32_e32 v74, v60
	v_mov_b32_e32 v75, v60
	v_mov_b32_e32 v76, v60
	v_mov_b32_e32 v77, v60
	v_mov_b32_e32 v78, v60
	v_mov_b32_e32 v79, v60
	v_mov_b32_e32 v80, v60
	v_mov_b32_e32 v81, v60
	v_mov_b32_e32 v82, v60
	v_mov_b32_e32 v83, v60
	v_mov_b32_e32 v84, v60
	v_mov_b32_e32 v85, v60
	s_branch .LBB0_1391
.LBB0_1391:
	s_add_i32 s19, s17, -1
	s_min_u32 s10, s19, 60
	s_mulk_i32 s10, 0x5900
	s_add_u32 s10, s4, s10
	s_addc_u32 s11, s5, 0
	s_add_u32 s12, s10, s14
	s_addc_u32 s13, s11, 0
	s_add_u32 s12, s12, 0x10b00
	s_addc_u32 s13, s13, 0
	v_lshl_add_u64 v[102:103], s[12:13], 0, v[106:107]
	v_add_co_u32_e32 v90, vcc, 0x1000, v102
	v_addc_co_u32_e32 v91, vcc, 0, v103, vcc
	v_add_co_u32_e32 v86, vcc, 0x2000, v102
	s_nop 0
	v_addc_co_u32_e32 v87, vcc, 0, v103, vcc
	v_add_co_u32_e32 v98, vcc, 0x3000, v102
	s_nop 0
	v_addc_co_u32_e32 v99, vcc, 0, v103, vcc
	global_load_dwordx4 v[94:97], v[102:103], off nt
	s_nop 0
	global_load_dwordx4 v[90:93], v[90:91], off nt
	s_nop 0
	global_load_dwordx4 v[86:89], v[86:87], off nt
	s_nop 0
	global_load_dwordx4 v[98:101], v[98:99], off nt
	s_and_b64 vcc, exec, s[38:39]
	s_cbranch_vccnz .LBB0_1393
	v_add_co_u32_e32 v70, vcc, 0x4000, v102
	s_nop 1
	v_addc_co_u32_e32 v71, vcc, 0, v103, vcc
	global_load_dwordx4 v[70:73], v[70:71], off nt
.LBB0_1393:
	s_and_saveexec_b64 s[12:13], s[6:7]
	s_cbranch_execz .LBB0_1395
	v_lshl_add_u64 v[66:67], s[10:11], 0, v[106:107]
	v_add_co_u32_e32 v66, vcc, 0x16000, v66
	s_nop 1
	v_addc_co_u32_e32 v67, vcc, 0, v67, vcc
	global_load_dwordx4 v[66:69], v[66:67], off offset:768 nt
.LBB0_1395:
	s_or_b64 exec, exec, s[12:13]
	s_min_u32 s10, s19, 61
	s_mulk_i32 s10, 0x5900
	s_add_u32 s10, s4, s10
	s_addc_u32 s11, s5, 0
	s_bitcmp1_b32 s19, 0
	s_cselect_b32 s12, 0x4a00, 0
	s_add_i32 s12, s15, s12
	v_add_u32_e32 v64, s12, v106
	ds_read_b128 v[102:105], v64
	ds_read_b128 v[120:123], v64 offset:1024
	ds_read_b128 v[124:127], v64 offset:2048
	ds_read_b128 v[128:131], v64 offset:3072
	ds_read_b128 v[132:135], v64 offset:4096
	ds_read_b128 v[136:139], v64 offset:5120
	ds_read_b128 v[140:143], v64 offset:6144
	ds_read_b128 v[144:147], v64 offset:7168
	ds_read_b128 v[148:151], v64 offset:8192
	ds_read_b128 v[152:155], v64 offset:9216
	ds_read_b128 v[156:159], v64 offset:10240
	ds_read_b128 v[160:163], v64 offset:11264
	ds_read_b128 v[172:175], v64 offset:12288
	ds_read_b128 v[176:179], v64 offset:13312
	ds_read_b128 v[180:183], v64 offset:14336
	ds_read_b128 v[184:187], v64 offset:15360
	ds_read_b128 v[188:191], v64 offset:16384
	ds_read_b128 v[192:195], v64 offset:17408
	v_add_u32_e32 v64, s12, v119
	ds_read_b128 v[196:199], v64 offset:18432
	ds_read_b128 v[200:203], v64 offset:18496
	ds_read_b128 v[204:207], v64 offset:18560
	ds_read_b128 v[208:211], v64 offset:18624
	v_cvt_pk_bf16_f32 v220, v60, v61
	v_cvt_pk_bf16_f32 v221, v62, v63
	s_waitcnt lgkmcnt(3)
	v_pk_mul_f32 v[62:63], v[62:63], v[198:199]
	v_pk_mul_f32 v[60:61], v[60:61], v[196:197]
	s_add_u32 s10, s10, s16
	v_cvt_pk_bf16_f32 v222, v74, v75
	s_waitcnt vmcnt(25)
	v_mfma_f32_16x16x32_bf16 v[60:63], v[180:183], v[56:59], v[60:63]
	v_cvt_pk_bf16_f32 v223, v76, v77
	s_addc_u32 s11, s11, 0
	v_cvt_pk_bf16_f32 v180, v78, v79
	v_mfma_f32_16x16x32_bf16 v[132:135], v[132:135], v[56:59], v[52:55]
	v_cvt_pk_bf16_f32 v181, v80, v81
	v_cvt_pk_bf16_f32 v182, v82, v83
	v_cvt_pk_bf16_f32 v183, v84, v85
	v_mfma_f32_16x16x32_bf16 v[60:63], v[140:143], v[220:223], v[60:63]
	v_lshl_add_u64 v[140:141], s[10:11], 0, v[106:107]
	s_mov_b32 s10, 0xb000
	v_add_co_u32_e32 v140, vcc, s10, v140
	v_mfma_f32_16x16x32_bf16 v[132:135], v[102:105], v[220:223], v[132:135]
	s_nop 0
	v_addc_co_u32_e32 v141, vcc, 0, v141, vcc
	global_load_dwordx4 v[102:105], v[140:141], off offset:512 nt
	v_mfma_f32_16x16x32_bf16 v[136:139], v[136:139], v[56:59], v[52:55]
	s_waitcnt lgkmcnt(2)
	v_pk_mul_f32 v[76:77], v[76:77], v[202:203]
	v_pk_mul_f32 v[74:75], v[74:75], v[200:201]
	s_waitcnt lgkmcnt(1)
	v_pk_mul_f32 v[80:81], v[80:81], v[206:207]
	v_mfma_f32_16x16x32_bf16 v[124:127], v[124:127], v[220:223], v[136:139]
	v_mul_f32_e64 v78, v78, v204
	v_mul_f32_e64 v79, v79, v205
	s_waitcnt lgkmcnt(0)
	v_pk_mul_f32 v[84:85], v[84:85], v[210:211]
	v_pk_mul_f32 v[82:83], v[82:83], v[208:209]
	v_mfma_f32_16x16x32_bf16 v[120:123], v[120:123], v[180:183], v[132:135]
	s_bitcmp1_b32 s17, 0
	s_cselect_b32 s10, 0x4a00, 0
	s_and_b64 vcc, exec, s[38:39]
	v_mfma_f32_16x16x32_bf16 v[124:127], v[128:131], v[180:183], v[124:127]
	v_lshl_add_u64 v[128:129], v[108:109], 0, s[8:9]
	s_nop 2
	v_bfe_u32 v64, v120, 16, 1
	v_add3_u32 v64, v120, v64, s30
	global_store_short_d16_hi v[128:129], v64, off offset:-2048
	v_lshl_add_u64 v[130:131], v[114:115], 0, s[8:9]
	v_bfe_u32 v64, v124, 16, 1
	v_add3_u32 v64, v124, v64, s30
	global_store_short_d16_hi v[130:131], v64, off
	v_bfe_u32 v64, v121, 16, 1
	v_add3_u32 v64, v121, v64, s30
	global_store_short_d16_hi v[128:129], v64, off offset:-1024
	v_bfe_u32 v64, v125, 16, 1
	v_add3_u32 v64, v125, v64, s30
	v_lshl_add_u64 v[120:121], v[116:117], 0, s[8:9]
	v_mfma_f32_16x16x32_bf16 v[74:77], v[184:187], v[56:59], v[74:77]
	global_store_short_d16_hi v[120:121], v64, off
	v_bfe_u32 v64, v122, 16, 1
	v_add3_u32 v64, v122, v64, s30
	v_mfma_f32_16x16x32_bf16 v[78:81], v[188:191], v[56:59], v[78:81]
	global_store_short_d16_hi v[128:129], v64, off
	v_bfe_u32 v64, v126, 16, 1
	v_add3_u32 v64, v126, v64, s30
	v_mfma_f32_16x16x32_bf16 v[56:59], v[192:195], v[56:59], v[82:85]
	v_lshl_add_u64 v[120:121], v[112:113], 0, s[8:9]
	global_store_short_d16_hi v[120:121], v64, off
	v_bfe_u32 v64, v123, 16, 1
	v_mfma_f32_16x16x32_bf16 v[74:77], v[148:151], v[220:223], v[74:77]
	v_add3_u32 v64, v123, v64, s30
	global_store_short_d16_hi v[128:129], v64, off offset:1024
	v_bfe_u32 v64, v127, 16, 1
	v_mfma_f32_16x16x32_bf16 v[78:81], v[156:159], v[220:223], v[78:81]
	v_add3_u32 v64, v127, v64, s30
	v_lshl_add_u64 v[82:83], v[110:111], 0, s[8:9]
	global_store_short_d16_hi v[82:83], v64, off
	v_mfma_f32_16x16x32_bf16 v[56:59], v[172:175], v[220:223], v[56:59]
	v_mfma_f32_16x16x32_bf16 v[60:63], v[144:147], v[180:183], v[60:63]
	v_mfma_f32_16x16x32_bf16 v[74:77], v[152:155], v[180:183], v[74:77]
	v_mfma_f32_16x16x32_bf16 v[78:81], v[160:163], v[180:183], v[78:81]
	v_mfma_f32_16x16x32_bf16 v[82:85], v[176:179], v[180:183], v[56:59]
	s_nop 3
	s_waitcnt vmcnt(35)
	v_add_u32_e32 v56, s10, v118
	v_add_u32_e32 v57, s14, v56
	ds_write_b128 v57, v[8:11]
	ds_write_b128 v57, v[12:15] offset:4096
	ds_write_b128 v57, v[20:23] offset:8192
	ds_write_b128 v57, v[16:19] offset:12288
	s_cbranch_vccnz .LBB0_1397
	ds_write_b128 v57, v[0:3] offset:16384

.Lr1_b1391:
	s_add_i32 s19, s17, -1
	s_min_u32 s10, s19, 60
	s_mulk_i32 s10, 0x5900
	s_add_u32 s10, s4, s10
	s_addc_u32 s11, s5, 0
	s_add_u32 s12, s10, s14
	s_addc_u32 s13, s11, 0
	s_add_u32 s12, s12, 0x10b00
	s_addc_u32 s13, s13, 0
	v_lshl_add_u64 v[56:57], s[12:13], 0, v[106:107]
	v_add_co_u32_e32 v12, vcc, 0x1000, v56
	v_addc_co_u32_e32 v13, vcc, 0, v57, vcc
	v_add_co_u32_e32 v20, vcc, 0x2000, v56
	s_nop 0
	v_addc_co_u32_e32 v21, vcc, 0, v57, vcc
	v_add_co_u32_e32 v16, vcc, 0x3000, v56
	s_nop 0
	v_addc_co_u32_e32 v17, vcc, 0, v57, vcc
	global_load_dwordx4 v[8:11], v[56:57], off nt
	s_nop 0
	global_load_dwordx4 v[12:15], v[12:13], off nt
	s_nop 0
	global_load_dwordx4 v[20:23], v[20:21], off nt
	s_nop 0
	global_load_dwordx4 v[16:19], v[16:17], off nt
	s_and_b64 vcc, exec, s[38:39]
	s_cbranch_vccnz .Lr1_b1393
	v_add_co_u32_e32 v0, vcc, 0x4000, v56
	s_nop 1
	v_addc_co_u32_e32 v1, vcc, 0, v57, vcc
	global_load_dwordx4 v[0:3], v[0:1], off nt
.Lr1_b1393:
	s_and_saveexec_b64 s[12:13], s[6:7]
	s_cbranch_execz .Lr1_b1395
	v_lshl_add_u64 v[4:5], s[10:11], 0, v[106:107]
	v_add_co_u32_e32 v4, vcc, 0x16000, v4
	s_nop 1
	v_addc_co_u32_e32 v5, vcc, 0, v5, vcc
	global_load_dwordx4 v[4:7], v[4:5], off offset:768 nt
.Lr1_b1395:
	s_or_b64 exec, exec, s[12:13]
	s_min_u32 s10, s19, 61
	s_mulk_i32 s10, 0x5900
	s_add_u32 s10, s4, s10
	s_addc_u32 s11, s5, 0
	s_bitcmp1_b32 s19, 0
	s_cselect_b32 s12, 0x4a00, 0
	s_add_i32 s12, s15, s12
	v_add_u32_e32 v64, s12, v106
	ds_read_b128 v[56:59], v64
	ds_read_b128 v[120:123], v64 offset:1024
	ds_read_b128 v[124:127], v64 offset:2048
	ds_read_b128 v[128:131], v64 offset:3072
	ds_read_b128 v[132:135], v64 offset:4096
	ds_read_b128 v[136:139], v64 offset:5120
	ds_read_b128 v[140:143], v64 offset:6144
	ds_read_b128 v[144:147], v64 offset:7168
	ds_read_b128 v[148:151], v64 offset:8192
	ds_read_b128 v[152:155], v64 offset:9216
	ds_read_b128 v[156:159], v64 offset:10240
	ds_read_b128 v[160:163], v64 offset:11264
	ds_read_b128 v[172:175], v64 offset:12288
	ds_read_b128 v[176:179], v64 offset:13312
	ds_read_b128 v[180:183], v64 offset:14336
	ds_read_b128 v[184:187], v64 offset:15360
	ds_read_b128 v[188:191], v64 offset:16384
	ds_read_b128 v[192:195], v64 offset:17408
	v_add_u32_e32 v64, s12, v119
	ds_read_b128 v[196:199], v64 offset:18432
	ds_read_b128 v[200:203], v64 offset:18496
	ds_read_b128 v[204:207], v64 offset:18560
	ds_read_b128 v[208:211], v64 offset:18624
	v_cvt_pk_bf16_f32 v220, v60, v61
	v_cvt_pk_bf16_f32 v221, v62, v63
	s_waitcnt lgkmcnt(3)
	v_pk_mul_f32 v[62:63], v[62:63], v[198:199]
	v_pk_mul_f32 v[60:61], v[60:61], v[196:197]
	s_add_u32 s10, s10, s16
	v_cvt_pk_bf16_f32 v222, v74, v75
	s_waitcnt vmcnt(25)
	v_mfma_f32_16x16x32_bf16 v[60:63], v[180:183], v[48:51], v[60:63]
	v_cvt_pk_bf16_f32 v223, v76, v77
	s_addc_u32 s11, s11, 0
	v_cvt_pk_bf16_f32 v180, v78, v79
	v_mfma_f32_16x16x32_bf16 v[132:135], v[132:135], v[48:51], v[52:55]
	v_cvt_pk_bf16_f32 v181, v80, v81
	v_cvt_pk_bf16_f32 v182, v82, v83
	v_cvt_pk_bf16_f32 v183, v84, v85
	v_mfma_f32_16x16x32_bf16 v[60:63], v[140:143], v[220:223], v[60:63]
	v_lshl_add_u64 v[140:141], s[10:11], 0, v[106:107]
	s_mov_b32 s10, 0xb000
	v_add_co_u32_e32 v140, vcc, s10, v140
	v_mfma_f32_16x16x32_bf16 v[132:135], v[56:59], v[220:223], v[132:135]
	s_nop 0
	v_addc_co_u32_e32 v141, vcc, 0, v141, vcc
	global_load_dwordx4 v[56:59], v[140:141], off offset:512 nt
	v_mfma_f32_16x16x32_bf16 v[136:139], v[136:139], v[48:51], v[52:55]
	s_waitcnt lgkmcnt(2)
	v_pk_mul_f32 v[76:77], v[76:77], v[202:203]
	v_pk_mul_f32 v[74:75], v[74:75], v[200:201]
	s_waitcnt lgkmcnt(1)
	v_pk_mul_f32 v[80:81], v[80:81], v[206:207]
	v_mfma_f32_16x16x32_bf16 v[124:127], v[124:127], v[220:223], v[136:139]
	v_mul_f32_e64 v78, v78, v204
	v_mul_f32_e64 v79, v79, v205
	s_waitcnt lgkmcnt(0)
	v_pk_mul_f32 v[84:85], v[84:85], v[210:211]
	v_pk_mul_f32 v[82:83], v[82:83], v[208:209]
	v_mfma_f32_16x16x32_bf16 v[120:123], v[120:123], v[180:183], v[132:135]
	s_bitcmp1_b32 s17, 0
	s_cselect_b32 s10, 0x4a00, 0
	s_and_b64 vcc, exec, s[38:39]
	v_mfma_f32_16x16x32_bf16 v[124:127], v[128:131], v[180:183], v[124:127]
	v_lshl_add_u64 v[128:129], v[108:109], 0, s[8:9]
	s_nop 2
	v_bfe_u32 v64, v120, 16, 1
	v_add3_u32 v64, v120, v64, s30
	global_store_short_d16_hi v[128:129], v64, off offset:-2048
	v_lshl_add_u64 v[130:131], v[114:115], 0, s[8:9]
	v_bfe_u32 v64, v124, 16, 1
	v_add3_u32 v64, v124, v64, s30
	global_store_short_d16_hi v[130:131], v64, off
	v_bfe_u32 v64, v121, 16, 1
	v_add3_u32 v64, v121, v64, s30
	global_store_short_d16_hi v[128:129], v64, off offset:-1024
	v_bfe_u32 v64, v125, 16, 1
	v_add3_u32 v64, v125, v64, s30
	v_lshl_add_u64 v[120:121], v[116:117], 0, s[8:9]
	v_mfma_f32_16x16x32_bf16 v[74:77], v[184:187], v[48:51], v[74:77]
	global_store_short_d16_hi v[120:121], v64, off
	v_bfe_u32 v64, v122, 16, 1
	v_add3_u32 v64, v122, v64, s30
	v_mfma_f32_16x16x32_bf16 v[78:81], v[188:191], v[48:51], v[78:81]
	global_store_short_d16_hi v[128:129], v64, off
	v_bfe_u32 v64, v126, 16, 1
	v_add3_u32 v64, v126, v64, s30
	v_mfma_f32_16x16x32_bf16 v[48:51], v[192:195], v[48:51], v[82:85]
	v_lshl_add_u64 v[120:121], v[112:113], 0, s[8:9]
	global_store_short_d16_hi v[120:121], v64, off
	v_bfe_u32 v64, v123, 16, 1
	v_mfma_f32_16x16x32_bf16 v[74:77], v[148:151], v[220:223], v[74:77]
	v_add3_u32 v64, v123, v64, s30
	global_store_short_d16_hi v[128:129], v64, off offset:1024
	v_bfe_u32 v64, v127, 16, 1
	v_mfma_f32_16x16x32_bf16 v[78:81], v[156:159], v[220:223], v[78:81]
	v_add3_u32 v64, v127, v64, s30
	v_lshl_add_u64 v[82:83], v[110:111], 0, s[8:9]
	global_store_short_d16_hi v[82:83], v64, off
	v_mfma_f32_16x16x32_bf16 v[48:51], v[172:175], v[220:223], v[48:51]
	v_mfma_f32_16x16x32_bf16 v[60:63], v[144:147], v[180:183], v[60:63]
	v_mfma_f32_16x16x32_bf16 v[74:77], v[152:155], v[180:183], v[74:77]
	v_mfma_f32_16x16x32_bf16 v[78:81], v[160:163], v[180:183], v[78:81]
	v_mfma_f32_16x16x32_bf16 v[82:85], v[176:179], v[180:183], v[48:51]
	s_nop 3
	s_waitcnt vmcnt(35)
	v_add_u32_e32 v48, s10, v118
	v_add_u32_e32 v49, s14, v48
	ds_write_b128 v49, v[28:31]
	ds_write_b128 v49, v[32:35] offset:4096
	ds_write_b128 v49, v[44:47] offset:8192
	ds_write_b128 v49, v[24:27] offset:12288
	s_cbranch_vccnz .Lr1_b1397
	ds_write_b128 v49, v[36:39] offset:16384

.Lr2_b1391:
	s_add_i32 s19, s17, -1
	s_min_u32 s10, s19, 60
	s_mulk_i32 s10, 0x5900
	s_add_u32 s10, s4, s10
	s_addc_u32 s11, s5, 0
	s_add_u32 s12, s10, s14
	s_addc_u32 s13, s11, 0
	s_add_u32 s12, s12, 0x10b00
	s_addc_u32 s13, s13, 0
	v_lshl_add_u64 v[48:49], s[12:13], 0, v[106:107]
	v_add_co_u32_e32 v32, vcc, 0x1000, v48
	v_addc_co_u32_e32 v33, vcc, 0, v49, vcc
	v_add_co_u32_e32 v44, vcc, 0x2000, v48
	s_nop 0
	v_addc_co_u32_e32 v45, vcc, 0, v49, vcc
	v_add_co_u32_e32 v24, vcc, 0x3000, v48
	s_nop 0
	v_addc_co_u32_e32 v25, vcc, 0, v49, vcc
	global_load_dwordx4 v[28:31], v[48:49], off nt
	s_nop 0
	global_load_dwordx4 v[32:35], v[32:33], off nt
	s_nop 0
	global_load_dwordx4 v[44:47], v[44:45], off nt
	s_nop 0
	global_load_dwordx4 v[24:27], v[24:25], off nt
	s_and_b64 vcc, exec, s[38:39]
	s_cbranch_vccnz .Lr2_b1393
	v_add_co_u32_e32 v36, vcc, 0x4000, v48
	s_nop 1
	v_addc_co_u32_e32 v37, vcc, 0, v49, vcc
	global_load_dwordx4 v[36:39], v[36:37], off nt
.Lr2_b1393:
	s_and_saveexec_b64 s[12:13], s[6:7]
	s_cbranch_execz .Lr2_b1395
	v_lshl_add_u64 v[40:41], s[10:11], 0, v[106:107]
	v_add_co_u32_e32 v40, vcc, 0x16000, v40
	s_nop 1
	v_addc_co_u32_e32 v41, vcc, 0, v41, vcc
	global_load_dwordx4 v[40:43], v[40:41], off offset:768 nt
.Lr2_b1395:
	s_or_b64 exec, exec, s[12:13]
	s_min_u32 s10, s19, 61
	s_mulk_i32 s10, 0x5900
	s_add_u32 s10, s4, s10
	s_addc_u32 s11, s5, 0
	s_bitcmp1_b32 s19, 0
	s_cselect_b32 s12, 0x4a00, 0
	s_add_i32 s12, s15, s12
	v_add_u32_e32 v64, s12, v106
	ds_read_b128 v[48:51], v64
	ds_read_b128 v[120:123], v64 offset:1024
	ds_read_b128 v[124:127], v64 offset:2048
	ds_read_b128 v[128:131], v64 offset:3072
	ds_read_b128 v[132:135], v64 offset:4096
	ds_read_b128 v[136:139], v64 offset:5120
	ds_read_b128 v[140:143], v64 offset:6144
	ds_read_b128 v[144:147], v64 offset:7168
	ds_read_b128 v[148:151], v64 offset:8192
	ds_read_b128 v[152:155], v64 offset:9216
	ds_read_b128 v[156:159], v64 offset:10240
	ds_read_b128 v[160:163], v64 offset:11264
	ds_read_b128 v[172:175], v64 offset:12288
	ds_read_b128 v[176:179], v64 offset:13312
	ds_read_b128 v[180:183], v64 offset:14336
	ds_read_b128 v[184:187], v64 offset:15360
	ds_read_b128 v[188:191], v64 offset:16384
	ds_read_b128 v[192:195], v64 offset:17408
	v_add_u32_e32 v64, s12, v119
	ds_read_b128 v[196:199], v64 offset:18432
	ds_read_b128 v[200:203], v64 offset:18496
	ds_read_b128 v[204:207], v64 offset:18560
	ds_read_b128 v[208:211], v64 offset:18624
	v_cvt_pk_bf16_f32 v220, v60, v61
	v_cvt_pk_bf16_f32 v221, v62, v63
	s_waitcnt lgkmcnt(3)
	v_pk_mul_f32 v[62:63], v[62:63], v[198:199]
	v_pk_mul_f32 v[60:61], v[60:61], v[196:197]
	s_add_u32 s10, s10, s16
	v_cvt_pk_bf16_f32 v222, v74, v75
	s_waitcnt vmcnt(25)
	v_mfma_f32_16x16x32_bf16 v[60:63], v[180:183], v[102:105], v[60:63]
	v_cvt_pk_bf16_f32 v223, v76, v77
	s_addc_u32 s11, s11, 0
	v_cvt_pk_bf16_f32 v180, v78, v79
	v_mfma_f32_16x16x32_bf16 v[132:135], v[132:135], v[102:105], v[52:55]
	v_cvt_pk_bf16_f32 v181, v80, v81
	v_cvt_pk_bf16_f32 v182, v82, v83
	v_cvt_pk_bf16_f32 v183, v84, v85
	v_mfma_f32_16x16x32_bf16 v[60:63], v[140:143], v[220:223], v[60:63]
	v_lshl_add_u64 v[140:141], s[10:11], 0, v[106:107]
	s_mov_b32 s10, 0xb000
	v_add_co_u32_e32 v140, vcc, s10, v140
	v_mfma_f32_16x16x32_bf16 v[132:135], v[48:51], v[220:223], v[132:135]
	s_nop 0
	v_addc_co_u32_e32 v141, vcc, 0, v141, vcc
	global_load_dwordx4 v[48:51], v[140:141], off offset:512 nt
	v_mfma_f32_16x16x32_bf16 v[136:139], v[136:139], v[102:105], v[52:55]
	s_waitcnt lgkmcnt(2)
	v_pk_mul_f32 v[76:77], v[76:77], v[202:203]
	v_pk_mul_f32 v[74:75], v[74:75], v[200:201]
	s_waitcnt lgkmcnt(1)
	v_pk_mul_f32 v[80:81], v[80:81], v[206:207]
	v_mfma_f32_16x16x32_bf16 v[124:127], v[124:127], v[220:223], v[136:139]
	v_mul_f32_e64 v78, v78, v204
	v_mul_f32_e64 v79, v79, v205
	s_waitcnt lgkmcnt(0)
	v_pk_mul_f32 v[84:85], v[84:85], v[210:211]
	v_pk_mul_f32 v[82:83], v[82:83], v[208:209]
	v_mfma_f32_16x16x32_bf16 v[120:123], v[120:123], v[180:183], v[132:135]
	s_bitcmp1_b32 s17, 0
	s_cselect_b32 s10, 0x4a00, 0
	s_and_b64 vcc, exec, s[38:39]
	v_mfma_f32_16x16x32_bf16 v[124:127], v[128:131], v[180:183], v[124:127]
	v_lshl_add_u64 v[128:129], v[108:109], 0, s[8:9]
	s_nop 2
	v_bfe_u32 v64, v120, 16, 1
	v_add3_u32 v64, v120, v64, s30
	global_store_short_d16_hi v[128:129], v64, off offset:-2048
	v_lshl_add_u64 v[130:131], v[114:115], 0, s[8:9]
	v_bfe_u32 v64, v124, 16, 1
	v_add3_u32 v64, v124, v64, s30
	global_store_short_d16_hi v[130:131], v64, off
	v_bfe_u32 v64, v121, 16, 1
	v_add3_u32 v64, v121, v64, s30
	global_store_short_d16_hi v[128:129], v64, off offset:-1024
	v_bfe_u32 v64, v125, 16, 1
	v_add3_u32 v64, v125, v64, s30
	v_lshl_add_u64 v[120:121], v[116:117], 0, s[8:9]
	v_mfma_f32_16x16x32_bf16 v[74:77], v[184:187], v[102:105], v[74:77]
	global_store_short_d16_hi v[120:121], v64, off
	v_bfe_u32 v64, v122, 16, 1
	v_add3_u32 v64, v122, v64, s30
	v_mfma_f32_16x16x32_bf16 v[78:81], v[188:191], v[102:105], v[78:81]
	global_store_short_d16_hi v[128:129], v64, off
	v_bfe_u32 v64, v126, 16, 1
	v_add3_u32 v64, v126, v64, s30
	v_mfma_f32_16x16x32_bf16 v[102:105], v[192:195], v[102:105], v[82:85]
	v_lshl_add_u64 v[120:121], v[112:113], 0, s[8:9]
	global_store_short_d16_hi v[120:121], v64, off
	v_bfe_u32 v64, v123, 16, 1
	v_mfma_f32_16x16x32_bf16 v[74:77], v[148:151], v[220:223], v[74:77]
	v_add3_u32 v64, v123, v64, s30
	global_store_short_d16_hi v[128:129], v64, off offset:1024
	v_bfe_u32 v64, v127, 16, 1
	v_mfma_f32_16x16x32_bf16 v[78:81], v[156:159], v[220:223], v[78:81]
	v_add3_u32 v64, v127, v64, s30
	v_lshl_add_u64 v[82:83], v[110:111], 0, s[8:9]
	global_store_short_d16_hi v[82:83], v64, off
	v_mfma_f32_16x16x32_bf16 v[102:105], v[172:175], v[220:223], v[102:105]
	v_mfma_f32_16x16x32_bf16 v[60:63], v[144:147], v[180:183], v[60:63]
	v_mfma_f32_16x16x32_bf16 v[74:77], v[152:155], v[180:183], v[74:77]
	v_mfma_f32_16x16x32_bf16 v[78:81], v[160:163], v[180:183], v[78:81]
	v_mfma_f32_16x16x32_bf16 v[82:85], v[176:179], v[180:183], v[102:105]
	s_nop 3
	s_waitcnt vmcnt(35)
	v_add_u32_e32 v102, s10, v118
	v_add_u32_e32 v103, s14, v102
	ds_write_b128 v103, v[94:97]
	ds_write_b128 v103, v[90:93] offset:4096
	ds_write_b128 v103, v[86:89] offset:8192
	ds_write_b128 v103, v[98:101] offset:12288
	s_cbranch_vccnz .Lr2_b1397
	ds_write_b128 v103, v[70:73] offset:16384

.LBB0_1401:
	s_lshl_b32 s4, s18, 1
	s_and_b32 s4, s4, 14
	s_and_b32 s5, s18, 0x70
	s_or_b32 s4, s5, s4
	s_bfe_u32 s5, s18, 0x10003
	s_or_b32 s4, s4, s5
	s_sub_i32 s19, s4, 32
	s_ashr_i32 s33, s19, 1
	s_mul_i32 s5, s33, 0x228000
	s_mul_hi_i32 s4, s33, 0x228000
	s_waitcnt lgkmcnt(0)
	s_add_u32 s5, s48, s5
	s_addc_u32 s6, s49, s4
	s_add_u32 s4, s5, 0xb4a00000
	s_addc_u32 s5, s6, 0
	s_cmp_lt_i32 s82, 18
	s_cselect_b64 s[10:11], -1, 0
	s_cmp_gt_i32 s82, 17
	s_cbranch_scc1 .LBB0_1403
	s_lshl_b32 s6, s82, 10
	s_ashr_i32 s7, s6, 31
	s_add_u32 s6, s4, s6
	s_waitcnt vmcnt(0)
	v_lshlrev_b32_e32 v0, 4, v227
	s_addc_u32 s7, s5, s7
	v_ashrrev_i32_e32 v1, 31, v0
	v_lshl_add_u64 v[0:1], s[6:7], 0, v[0:1]
	global_load_dwordx4 v[66:69], v[0:1], off nt
.LBB0_1403:
	s_cmp_lt_i32 s82, 10
	s_cselect_b64 s[12:13], -1, 0
	s_cmp_gt_i32 s82, 9
	s_cbranch_scc1 .LBB0_1405
	s_lshl_b32 s6, s82, 10
	s_addk_i32 s6, 0x2000
	s_ashr_i32 s7, s6, 31
	s_add_u32 s6, s4, s6
	s_waitcnt vmcnt(0)
	v_lshlrev_b32_e32 v0, 4, v227
	s_addc_u32 s7, s5, s7
	v_ashrrev_i32_e32 v1, 31, v0
	v_lshl_add_u64 v[0:1], s[6:7], 0, v[0:1]
	global_load_dwordx4 v[70:73], v[0:1], off nt
.LBB0_1405:
	s_cmp_lt_i32 s82, 2
	s_cselect_b64 s[14:15], -1, 0
	s_cmp_gt_i32 s82, 1
	s_cbranch_scc1 .LBB0_1407
	s_lshl_b32 s6, s82, 10
	s_addk_i32 s6, 0x4000
	s_ashr_i32 s7, s6, 31
	s_add_u32 s6, s4, s6
	s_waitcnt vmcnt(0)
	v_lshlrev_b32_e32 v0, 4, v227
	s_addc_u32 s7, s5, s7
	v_ashrrev_i32_e32 v1, 31, v0
	v_lshl_add_u64 v[0:1], s[6:7], 0, v[0:1]
	global_load_dwordx4 v[74:77], v[0:1], off nt
.LBB0_1407:
	s_cmp_eq_u32 s82, 7
	s_cselect_b64 s[6:7], -1, 0
	v_cmp_gt_i32_e32 vcc, 24, v227
	s_and_b64 s[6:7], s[6:7], vcc
	s_xor_b64 s[8:9], s[6:7], -1
	s_and_saveexec_b64 s[16:17], s[8:9]
	s_xor_b64 s[16:17], exec, s[16:17]
	v_lshlrev_b32_e32 v154, 4, v227
	s_or_saveexec_b64 s[16:17], s[16:17]
	s_xor_b64 exec, exec, s[16:17]
	s_cbranch_execz .LBB0_1411
	v_lshlrev_b32_e32 v154, 4, v227
	v_ashrrev_i32_e32 v155, 31, v154
	s_waitcnt vmcnt(0)
	v_lshl_add_u64 v[0:1], s[4:5], 0, v[154:155]
	v_add_co_u32_e32 v0, vcc, 0x8000, v0
	s_nop 1
	v_addc_co_u32_e32 v1, vcc, 0, v1, vcc
	global_load_dwordx4 v[78:81], v[0:1], off offset:2048 nt

.LBB0_1419:
	s_or_b64 exec, exec, s[10:11]
	s_add_u32 s14, s4, 0x8a00
	s_addc_u32 s15, s5, 0
	s_and_b64 vcc, exec, s[38:39]
	v_ashrrev_i32_e32 v155, 31, v154
	s_cbranch_vccnz .LBB0_1423
	s_lshl_b32 s10, s82, 10
	s_ashr_i32 s11, s10, 31
	s_add_u32 s10, s14, s10
	s_addc_u32 s11, s15, s11
	v_lshl_add_u64 v[0:1], s[10:11], 0, v[154:155]
	global_load_dwordx4 v[66:69], v[0:1], off nt
	s_and_b64 vcc, exec, s[40:41]
	s_cbranch_vccz .LBB0_1424

.LBB0_1422:
	s_lshl_b32 s10, s82, 10
	s_addk_i32 s10, 0x4000
	s_ashr_i32 s11, s10, 31
	s_add_u32 s10, s14, s10
	s_addc_u32 s11, s15, s11
	v_lshl_add_u64 v[0:1], s[10:11], 0, v[154:155]
	global_load_dwordx4 v[74:77], v[0:1], off nt
	s_and_saveexec_b64 s[10:11], s[6:7]
	s_cbranch_execnz .LBB0_1426
	s_branch .LBB0_1427

.LBB0_1424:
	s_lshl_b32 s10, s82, 10
	s_addk_i32 s10, 0x2000
	s_ashr_i32 s11, s10, 31
	s_add_u32 s10, s14, s10
	s_addc_u32 s11, s15, s11
	v_lshl_add_u64 v[0:1], s[10:11], 0, v[154:155]
	global_load_dwordx4 v[70:73], v[0:1], off nt
	s_and_b64 vcc, exec, s[42:43]
	s_cbranch_vccz .LBB0_1422

.LBB0_1426:
	v_lshl_add_u64 v[0:1], s[4:5], 0, v[154:155]
	v_add_co_u32_e32 v0, vcc, 0x11000, v0
	s_nop 1
	v_addc_co_u32_e32 v1, vcc, 0, v1, vcc
	global_load_dwordx4 v[78:81], v[0:1], off offset:512 nt
.LBB0_1427:
	s_or_b64 exec, exec, s[10:11]
	s_add_u32 s10, s4, 0x11400
	s_addc_u32 s11, s5, 0
	s_and_b64 vcc, exec, s[38:39]
	s_cbranch_vccnz .LBB0_1465
	s_lshl_b32 s12, s82, 10
	s_ashr_i32 s13, s12, 31
	s_add_u32 s12, s10, s12
	s_addc_u32 s13, s11, s13
	v_lshl_add_u64 v[0:1], s[12:13], 0, v[154:155]
	global_load_dwordx4 v[82:85], v[0:1], off nt
	s_and_b64 vcc, exec, s[40:41]
	s_cbranch_vccz .LBB0_1466

.LBB0_1430:
	s_lshl_b32 s12, s82, 10
	s_addk_i32 s12, 0x4000
	s_ashr_i32 s13, s12, 31
	s_add_u32 s10, s10, s12
	s_addc_u32 s11, s11, s13
	v_lshl_add_u64 v[0:1], s[10:11], 0, v[154:155]
	global_load_dwordx4 v[90:93], v[0:1], off nt
.LBB0_1431:
	s_and_saveexec_b64 s[10:11], s[8:9]
	s_xor_b64 s[8:9], exec, s[10:11]
	s_or_saveexec_b64 s[8:9], s[8:9]
	s_xor_b64 exec, exec, s[8:9]
	s_cbranch_execz .LBB0_1433
	v_lshl_add_u64 v[0:1], s[4:5], 0, v[154:155]
	v_add_co_u32_e32 v0, vcc, 0x19000, v0
	s_nop 1
	v_addc_co_u32_e32 v1, vcc, 0, v1, vcc
	global_load_dwordx4 v[94:97], v[0:1], off offset:3072 nt
.LBB0_1433:
	s_or_b64 exec, exec, s[8:9]
	s_cmp_lt_i32 s82, 4
	s_cselect_b64 s[8:9], -1, 0
	s_cmp_gt_i32 s82, 3
	s_cselect_b64 s[10:11], -1, 0
	s_lshl_b32 s17, s19, 2
	s_and_b32 s20, s82, 3
	s_ashr_i32 s16, s19, 3
	s_cmp_eq_u32 s82, 4
	s_cselect_b64 s[12:13], -1, 0
	s_and_b32 s17, s17, 4
	s_or_b32 s34, s17, s20
	v_ashrrev_i32_e32 v5, 4, v227
	s_lshl_b32 s17, s34, 11
	v_and_b32_e32 v4, 15, v227
	s_add_i32 s19, s17, 0x4c00
	v_lshlrev_b32_e32 v2, 3, v5
	s_mov_b32 s17, 0xffffff0
	s_add_u32 s20, s4, s19
	v_and_or_b32 v0, v2, s17, v4
	s_addc_u32 s21, s5, 0
	v_lshlrev_b32_e32 v174, 4, v0
	v_ashrrev_i32_e32 v175, 31, v174
	s_add_u32 s14, s14, s19
	v_lshl_add_u64 v[0:1], s[20:21], 0, v[174:175]
	v_and_b32_e32 v64, 8, v2
	s_addc_u32 s15, s15, 0
	v_lshl_add_u64 v[0:1], v[0:1], 0, v[64:65]
	v_lshl_add_u64 v[2:3], s[14:15], 0, v[174:175]
	global_load_dwordx2 v[146:147], v[0:1], off nt
	global_load_dwordx2 v[148:149], v[0:1], off offset:512 nt
	v_lshl_add_u64 v[0:1], s[20:21], 0, v[154:155]
	v_lshl_add_u64 v[2:3], v[2:3], 0, v[64:65]
	global_load_dwordx4 v[150:153], v[0:1], off nt
	global_load_dwordx2 v[98:99], v[2:3], off nt
	v_lshl_add_u64 v[0:1], s[14:15], 0, v[154:155]
	global_load_dwordx2 v[100:101], v[2:3], off offset:512 nt
	global_load_dwordx4 v[106:109], v[0:1], off nt
	s_lshl_b32 s20, s82, 10
	s_add_i32 s22, s20, 0x2000
	s_add_i32 s24, s20, 0x4000
	s_ashr_i32 s17, s16, 31
	s_ashr_i32 s21, s20, 31
	s_ashr_i32 s23, s22, 31
	s_ashr_i32 s25, s24, 31
	s_lshl_b64 s[14:15], s[16:17], 21
	s_add_u32 s14, s48, s14
	s_addc_u32 s15, s49, s15
	s_add_u32 s26, s14, 0x76200000
	s_addc_u32 s27, s15, 0
	s_lshl_b32 s14, s33, 7
	s_and_b32 s33, s14, 0x180
	s_lshl_b32 s14, s33, 1
	v_mov_b32_e32 v114, v65
	s_add_u32 s14, s26, s14
	s_waitcnt vmcnt(0) lgkmcnt(0)
	s_barrier
	s_addc_u32 s15, s27, 0
	v_mov_b32_e32 v115, v114
	v_mov_b32_e32 v116, v114
	v_mov_b32_e32 v117, v114
	s_lshl_b32 s50, s34, 4
	s_lshl_b32 s16, s34, 5
	v_mov_b32_e32 v118, 0x3f803f80
	v_lshl_or_b32 v176, v5, 11, v4
	s_add_u32 s52, s14, s16
	v_and_b32_e32 v0, -16, v227
	v_mov_b64_e32 v[140:141], v[116:117]
	v_mov_b64_e32 v[110:111], v[114:115]
	v_mov_b64_e32 v[144:145], v[116:117]
	v_mov_b64_e32 v[102:103], v[114:115]
	v_lshlrev_b32_e32 v183, 2, v5
	v_mov_b32_e32 v119, v118
	v_mov_b32_e32 v120, v118
	v_mov_b32_e32 v121, v118
	v_cmp_eq_u32_e64 s[44:45], 0, v4
	s_mov_b32 s51, 1
	s_addc_u32 s53, s15, 0
	v_mov_b32_e32 v177, v65
	v_add_u32_e32 v172, 0x2000, v176
	v_mov_b32_e32 v173, v65
	v_add_u32_e32 v160, 0x2200, v176
	v_mov_b32_e32 v161, v65
	v_add_u32_e32 v158, 0x2400, v176
	v_mov_b32_e32 v159, v65
	v_add_u32_e32 v156, 0x2600, v176
	v_mov_b32_e32 v157, v65
	v_add_u32_e32 v182, 0, v0
	v_mov_b32_e32 v0, v65
	v_mov_b32_e32 v1, v65
	v_mov_b32_e32 v2, v65
	v_mov_b32_e32 v3, v65
	v_mov_b32_e32 v4, v65
	v_mov_b32_e32 v5, v65
	v_mov_b32_e32 v6, v65
	v_mov_b32_e32 v7, v65
	v_mov_b32_e32 v8, v65
	v_mov_b32_e32 v9, v65
	v_mov_b32_e32 v10, v65
	v_mov_b32_e32 v11, v65
	v_mov_b32_e32 v12, v65
	v_mov_b32_e32 v13, v65
	v_mov_b32_e32 v14, v65
	v_mov_b32_e32 v15, v65
	v_mov_b32_e32 v16, v65
	v_mov_b32_e32 v17, v65
	v_mov_b32_e32 v18, v65
	v_mov_b32_e32 v19, v65
	v_mov_b32_e32 v20, v65
	v_mov_b32_e32 v21, v65
	v_mov_b32_e32 v22, v65
	v_mov_b32_e32 v23, v65
	v_mov_b32_e32 v24, v65
	v_mov_b32_e32 v25, v65
	v_mov_b32_e32 v26, v65
	v_mov_b32_e32 v27, v65
	v_mov_b32_e32 v28, v65
	v_mov_b32_e32 v29, v65
	v_mov_b32_e32 v30, v65
	v_mov_b32_e32 v31, v65
	s_movk_i32 s34, 0xffe0
	s_movk_i32 s54, 0xffc0
	v_mov_b32_e32 v185, 0xf149f2ca
	v_mov_b64_e32 v[138:139], v[114:115]
	v_mov_b64_e32 v[112:113], v[116:117]
	v_mov_b64_e32 v[142:143], v[114:115]
	v_mov_b64_e32 v[104:105], v[116:117]
.LBB0_1434:
	s_add_i32 s55, s51, -1
	s_min_u32 s14, s55, 60
	s_mul_i32 s14, s14, 0x8a00
	s_add_u32 s14, s4, s14
	s_addc_u32 s15, s5, 0
	s_add_u32 s16, s14, 0x19e00
	s_addc_u32 s17, s15, 0
	s_and_b64 vcc, exec, s[38:39]
	s_cbranch_vccnz .LBB0_1438
	s_add_u32 s56, s16, s20
	s_addc_u32 s57, s17, s21
	v_lshl_add_u64 v[32:33], s[56:57], 0, v[154:155]
	global_load_dwordx4 v[134:137], v[32:33], off nt
	s_and_b64 vcc, exec, s[40:41]
	s_cbranch_vccz .LBB0_1439

.LBB0_1437:
	s_add_u32 s16, s16, s24
	s_addc_u32 s17, s17, s25
	v_lshl_add_u64 v[32:33], s[16:17], 0, v[154:155]
	global_load_dwordx4 v[126:129], v[32:33], off nt
	s_and_saveexec_b64 s[16:17], s[6:7]
	s_cbranch_execnz .LBB0_1441
	s_branch .LBB0_1442

.LBB0_1439:
	s_add_u32 s56, s16, s22
	s_addc_u32 s57, s17, s23
	v_lshl_add_u64 v[32:33], s[56:57], 0, v[154:155]
	global_load_dwordx4 v[122:125], v[32:33], off nt
	s_and_b64 vcc, exec, s[42:43]
	s_cbranch_vccz .LBB0_1437

.LBB0_1441:
	v_lshl_add_u64 v[32:33], s[14:15], 0, v[154:155]
	v_add_co_u32_e32 v32, vcc, 0x22000, v32
	s_nop 1
	v_addc_co_u32_e32 v33, vcc, 0, v33, vcc
	global_load_dwordx4 v[130:133], v[32:33], off offset:1536 nt

.LBB0_1453:
	v_add_u32_e32 v185, s16, v154
	ds_read_b128 v[44:47], v185 offset:16384
	ds_read_b128 v[48:51], v185 offset:17408
	ds_read_b128 v[52:55], v185
	ds_read_b128 v[56:59], v185 offset:1024
	ds_read_b128 v[60:63], v185 offset:2048
	ds_read_b128 v[102:105], v185 offset:3072
	ds_read_b128 v[110:113], v185 offset:4096
	ds_read_b128 v[142:145], v185 offset:5120
	ds_read_b128 v[162:165], v185 offset:6144
	ds_read_b128 v[186:189], v185 offset:7168
	s_min_u32 s14, s55, 61
	s_mul_i32 s14, s14, 0x8a00
	s_add_u32 s14, s4, s14
	s_addc_u32 s15, s5, 0
	v_cvt_pk_bf16_f32 v32, v0, v1
	v_cvt_pk_bf16_f32 v33, v2, v3
	v_cvt_pk_bf16_f32 v34, v4, v5
	v_cvt_pk_bf16_f32 v35, v6, v7
	v_cvt_pk_bf16_f32 v36, v8, v9
	v_cvt_pk_bf16_f32 v37, v10, v11
	v_cvt_pk_bf16_f32 v38, v12, v13
	v_cvt_pk_bf16_f32 v39, v14, v15
	v_cvt_pk_bf16_f32 v40, v16, v17
	v_cvt_pk_bf16_f32 v41, v18, v19
	v_cvt_pk_bf16_f32 v42, v20, v21
	v_cvt_pk_bf16_f32 v43, v22, v23
	v_cvt_pk_bf16_f32 v190, v24, v25
	v_cvt_pk_bf16_f32 v191, v26, v27
	v_cvt_pk_bf16_f32 v192, v28, v29
	v_cvt_pk_bf16_f32 v193, v30, v31
	s_waitcnt vmcnt(23) lgkmcnt(9)
	v_mfma_f32_16x16x32_bf16 v[138:141], v[44:47], v[146:149], v[114:117]
	s_add_u32 s14, s14, s19
	s_addc_u32 s15, s15, 0
	s_add_u32 s14, s14, 0x11400
	s_waitcnt lgkmcnt(7)
	v_mfma_f32_16x16x32_bf16 v[44:47], v[52:55], v[32:35], v[114:117]
	s_addc_u32 s15, s15, 0
	s_waitcnt lgkmcnt(3)
	v_mfma_f32_16x16x32_bf16 v[32:35], v[110:113], v[32:35], v[114:117]
	v_mfma_f32_16x16x32_bf16 v[44:47], v[56:59], v[36:39], v[44:47]
	s_waitcnt lgkmcnt(2)
	v_mfma_f32_16x16x32_bf16 v[32:35], v[142:145], v[36:39], v[32:35]
	v_mfma_f32_16x16x32_bf16 v[36:39], v[60:63], v[40:43], v[44:47]
	s_nop 4
	s_nop 0
	s_nop 0
	s_waitcnt lgkmcnt(1)
	v_mfma_f32_16x16x32_bf16 v[40:43], v[162:165], v[40:43], v[32:35]
	s_nop 2
	s_nop 0
	s_nop 0
	v_mfma_f32_16x16x32_bf16 v[142:145], v[102:105], v[190:193], v[36:39]
	s_nop 2
	ds_read_b128 v[36:39], v185 offset:8192
	ds_read_b128 v[44:47], v185 offset:9216
	ds_read_b128 v[52:55], v185 offset:10240
	ds_read_b128 v[56:59], v185 offset:11264
	s_waitcnt lgkmcnt(4)
	v_mfma_f32_16x16x32_bf16 v[102:105], v[186:189], v[190:193], v[40:43]
	s_nop 2
	ds_read_b128 v[40:43], v185 offset:12288
	ds_read_b128 v[60:63], v185 offset:13312
	ds_read_b128 v[162:165], v185 offset:14336
	ds_read_b128 v[186:189], v185 offset:15360
	v_mfma_f32_16x16x32_bf16 v[110:113], v[48:51], v[146:149], v[114:117]
	s_waitcnt lgkmcnt(7)
	v_mfma_f32_16x16x32_bf16 v[36:39], v[36:39], v[150:153], v[114:117]
	s_waitcnt lgkmcnt(0)
	v_mfma_f32_16x16x32_bf16 v[146:149], v[186:189], v[150:153], v[114:117]
	v_mfma_f32_16x16x32_bf16 v[44:47], v[44:47], v[150:153], v[114:117]
	s_nop 4
	v_mul_f32_e64 v36, v180, v36
	v_mul_f32_e64 v37, v180, v37
	v_pk_mul_f32 v[38:39], v[180:181], v[38:39] op_sel_hi:[0,1]
	v_pk_fma_f32 v[0:1], v[0:1], v[178:179], v[36:37] op_sel_hi:[1,0,1]
	s_nop 0
	v_pk_fma_f32 v[2:3], v[2:3], v[178:179], v[38:39] op_sel_hi:[1,0,1]
	s_nop 0
	v_mfma_f32_16x16x32_bf16 v[48:51], v[52:55], v[150:153], v[114:117]
	v_mul_f32_e64 v148, v180, v148
	v_mul_f32_e64 v149, v180, v149
	v_pk_mul_f32 v[146:147], v[180:181], v[146:147] op_sel_hi:[0,1]
	v_pk_fma_f32 v[28:29], v[28:29], v[178:179], v[146:147] op_sel_hi:[1,0,1]
	v_mfma_f32_16x16x32_bf16 v[52:55], v[56:59], v[150:153], v[114:117]
	v_fma_f32 v30, v30, v178, v148
	v_fma_f32 v31, v31, v178, v149
	s_nop 0
	s_nop 0
	v_pk_mul_f32 v[46:47], v[180:181], v[46:47] op_sel_hi:[0,1]
	v_mfma_f32_16x16x32_bf16 v[40:43], v[40:43], v[150:153], v[114:117]
	v_mul_f32_e64 v50, v180, v50
	v_mul_f32_e64 v51, v180, v51
	v_pk_mul_f32 v[54:55], v[180:181], v[54:55] op_sel_hi:[0,1]
	v_pk_mul_f32 v[44:45], v[180:181], v[44:45] op_sel_hi:[0,1]
	v_mfma_f32_16x16x32_bf16 v[56:59], v[60:63], v[150:153], v[114:117]
	v_mul_f32_e64 v48, v180, v48
	v_mul_f32_e64 v49, v180, v49
	s_nop 0
	v_pk_mul_f32 v[42:43], v[180:181], v[42:43] op_sel_hi:[0,1]
	v_pk_mul_f32 v[52:53], v[180:181], v[52:53] op_sel_hi:[0,1]
	v_mfma_f32_16x16x32_bf16 v[60:63], v[162:165], v[150:153], v[114:117]
	s_nop 0
	s_nop 0
	v_pk_mul_f32 v[58:59], v[180:181], v[58:59] op_sel_hi:[0,1]
	v_pk_mul_f32 v[40:41], v[180:181], v[40:41] op_sel_hi:[0,1]
	v_pk_mul_f32 v[56:57], v[180:181], v[56:57] op_sel_hi:[0,1]
	s_nop 0
	s_nop 1
	v_pk_mul_f32 v[62:63], v[180:181], v[62:63] op_sel_hi:[0,1]
	v_pk_mul_f32 v[60:61], v[180:181], v[60:61] op_sel_hi:[0,1]
	s_nop 0
	s_nop 0
	s_nop 0
	v_pk_fma_f32 v[24:25], v[24:25], v[178:179], v[60:61] op_sel_hi:[1,0,1]
	v_pk_fma_f32 v[20:21], v[20:21], v[178:179], v[56:57] op_sel_hi:[1,0,1]
	v_pk_fma_f32 v[16:17], v[16:17], v[178:179], v[40:41] op_sel_hi:[1,0,1]
	v_pk_fma_f32 v[12:13], v[12:13], v[178:179], v[52:53] op_sel_hi:[1,0,1]
	v_pk_fma_f32 v[8:9], v[8:9], v[178:179], v[48:49] op_sel_hi:[1,0,1]
	v_pk_fma_f32 v[4:5], v[4:5], v[178:179], v[44:45] op_sel_hi:[1,0,1]
	v_pk_fma_f32 v[26:27], v[26:27], v[178:179], v[62:63] op_sel_hi:[1,0,1]
	v_pk_fma_f32 v[22:23], v[22:23], v[178:179], v[58:59] op_sel_hi:[1,0,1]
	v_pk_fma_f32 v[18:19], v[18:19], v[178:179], v[42:43] op_sel_hi:[1,0,1]
	v_pk_fma_f32 v[14:15], v[14:15], v[178:179], v[54:55] op_sel_hi:[1,0,1]
	v_pk_fma_f32 v[10:11], v[10:11], v[178:179], v[50:51] op_sel_hi:[1,0,1]
	v_pk_fma_f32 v[6:7], v[6:7], v[178:179], v[46:47] op_sel_hi:[1,0,1]
	s_nop 0
	s_nop 0
	v_lshl_add_u64 v[32:33], s[14:15], 0, v[174:175]
	v_lshl_add_u64 v[34:35], s[14:15], 0, v[154:155]
	v_lshl_add_u64 v[32:33], v[32:33], 0, v[64:65]
	global_load_dwordx2 v[200:201], v[32:33], off nt
	global_load_dwordx2 v[202:203], v[32:33], off offset:512 nt
	global_load_dwordx4 v[204:207], v[34:35], off nt
	s_branch .LBB0_1455

.Lm1_b1434:
	s_add_i32 s55, s51, -1
	s_min_u32 s14, s55, 60
	s_mul_i32 s14, s14, 0x8a00
	s_add_u32 s14, s4, s14
	s_addc_u32 s15, s5, 0
	s_add_u32 s16, s14, 0x19e00
	s_addc_u32 s17, s15, 0
	s_and_b64 vcc, exec, s[38:39]
	s_cbranch_vccnz .Lm1_b1438
	s_add_u32 s56, s16, s20
	s_addc_u32 s57, s17, s21
	v_lshl_add_u64 v[32:33], s[56:57], 0, v[154:155]
	global_load_dwordx4 v[66:69], v[32:33], off nt
	s_and_b64 vcc, exec, s[40:41]
	s_cbranch_vccz .Lm1_b1439

.Lm1_b1437:
	s_add_u32 s16, s16, s24
	s_addc_u32 s17, s17, s25
	v_lshl_add_u64 v[32:33], s[16:17], 0, v[154:155]
	global_load_dwordx4 v[74:77], v[32:33], off nt
	s_and_saveexec_b64 s[16:17], s[6:7]
	s_cbranch_execnz .Lm1_b1441
	s_branch .Lm1_b1442

.Lm1_b1439:
	s_add_u32 s56, s16, s22
	s_addc_u32 s57, s17, s23
	v_lshl_add_u64 v[32:33], s[56:57], 0, v[154:155]
	global_load_dwordx4 v[70:73], v[32:33], off nt
	s_and_b64 vcc, exec, s[42:43]
	s_cbranch_vccz .Lm1_b1437

.Lm1_b1441:
	v_lshl_add_u64 v[32:33], s[14:15], 0, v[154:155]
	v_add_co_u32_e32 v32, vcc, 0x22000, v32
	s_nop 1
	v_addc_co_u32_e32 v33, vcc, 0, v33, vcc
	global_load_dwordx4 v[78:81], v[32:33], off offset:1536 nt

.Lm1_b1453:
	v_add_u32_e32 v185, s16, v154
	ds_read_b128 v[44:47], v185 offset:16384
	ds_read_b128 v[48:51], v185 offset:17408
	ds_read_b128 v[52:55], v185
	ds_read_b128 v[56:59], v185 offset:1024
	ds_read_b128 v[60:63], v185 offset:2048
	ds_read_b128 v[102:105], v185 offset:3072
	ds_read_b128 v[110:113], v185 offset:4096
	ds_read_b128 v[142:145], v185 offset:5120
	ds_read_b128 v[162:165], v185 offset:6144
	ds_read_b128 v[186:189], v185 offset:7168
	s_min_u32 s14, s55, 61
	s_mul_i32 s14, s14, 0x8a00
	s_add_u32 s14, s4, s14
	s_addc_u32 s15, s5, 0
	v_cvt_pk_bf16_f32 v32, v0, v1
	v_cvt_pk_bf16_f32 v33, v2, v3
	v_cvt_pk_bf16_f32 v34, v4, v5
	v_cvt_pk_bf16_f32 v35, v6, v7
	v_cvt_pk_bf16_f32 v36, v8, v9
	v_cvt_pk_bf16_f32 v37, v10, v11
	v_cvt_pk_bf16_f32 v38, v12, v13
	v_cvt_pk_bf16_f32 v39, v14, v15
	v_cvt_pk_bf16_f32 v40, v16, v17
	v_cvt_pk_bf16_f32 v41, v18, v19
	v_cvt_pk_bf16_f32 v42, v20, v21
	v_cvt_pk_bf16_f32 v43, v22, v23
	v_cvt_pk_bf16_f32 v190, v24, v25
	v_cvt_pk_bf16_f32 v191, v26, v27
	v_cvt_pk_bf16_f32 v192, v28, v29
	v_cvt_pk_bf16_f32 v193, v30, v31
	s_waitcnt vmcnt(23) lgkmcnt(9)
	v_mfma_f32_16x16x32_bf16 v[138:141], v[44:47], v[98:101], v[114:117]
	s_add_u32 s14, s14, s19
	s_addc_u32 s15, s15, 0
	s_add_u32 s14, s14, 0x11400
	s_waitcnt lgkmcnt(7)
	v_mfma_f32_16x16x32_bf16 v[44:47], v[52:55], v[32:35], v[114:117]
	s_addc_u32 s15, s15, 0
	s_waitcnt lgkmcnt(3)
	v_mfma_f32_16x16x32_bf16 v[32:35], v[110:113], v[32:35], v[114:117]
	v_mfma_f32_16x16x32_bf16 v[44:47], v[56:59], v[36:39], v[44:47]
	s_waitcnt lgkmcnt(2)
	v_mfma_f32_16x16x32_bf16 v[32:35], v[142:145], v[36:39], v[32:35]
	v_mfma_f32_16x16x32_bf16 v[36:39], v[60:63], v[40:43], v[44:47]
	s_nop 4
	s_nop 0
	s_nop 0
	s_waitcnt lgkmcnt(1)
	v_mfma_f32_16x16x32_bf16 v[40:43], v[162:165], v[40:43], v[32:35]
	s_nop 2
	s_nop 0
	s_nop 0
	v_mfma_f32_16x16x32_bf16 v[142:145], v[102:105], v[190:193], v[36:39]
	s_nop 2
	ds_read_b128 v[36:39], v185 offset:8192
	ds_read_b128 v[44:47], v185 offset:9216
	ds_read_b128 v[52:55], v185 offset:10240
	ds_read_b128 v[56:59], v185 offset:11264
	s_waitcnt lgkmcnt(4)
	v_mfma_f32_16x16x32_bf16 v[102:105], v[186:189], v[190:193], v[40:43]
	s_nop 2
	ds_read_b128 v[40:43], v185 offset:12288
	ds_read_b128 v[60:63], v185 offset:13312
	ds_read_b128 v[162:165], v185 offset:14336
	ds_read_b128 v[186:189], v185 offset:15360
	v_mfma_f32_16x16x32_bf16 v[110:113], v[48:51], v[98:101], v[114:117]
	s_waitcnt lgkmcnt(7)
	v_mfma_f32_16x16x32_bf16 v[36:39], v[36:39], v[106:109], v[114:117]
	s_waitcnt lgkmcnt(0)
	v_mfma_f32_16x16x32_bf16 v[98:101], v[186:189], v[106:109], v[114:117]
	v_mfma_f32_16x16x32_bf16 v[44:47], v[44:47], v[106:109], v[114:117]
	s_nop 4
	v_mul_f32_e64 v36, v180, v36
	v_mul_f32_e64 v37, v180, v37
	v_pk_mul_f32 v[38:39], v[180:181], v[38:39] op_sel_hi:[0,1]
	v_pk_fma_f32 v[0:1], v[0:1], v[178:179], v[36:37] op_sel_hi:[1,0,1]
	s_nop 0
	v_pk_fma_f32 v[2:3], v[2:3], v[178:179], v[38:39] op_sel_hi:[1,0,1]
	s_nop 0
	v_mfma_f32_16x16x32_bf16 v[48:51], v[52:55], v[106:109], v[114:117]
	v_mul_f32_e64 v100, v180, v100
	v_mul_f32_e64 v101, v180, v101
	v_pk_mul_f32 v[98:99], v[180:181], v[98:99] op_sel_hi:[0,1]
	v_pk_fma_f32 v[28:29], v[28:29], v[178:179], v[98:99] op_sel_hi:[1,0,1]
	v_mfma_f32_16x16x32_bf16 v[52:55], v[56:59], v[106:109], v[114:117]
	v_fma_f32 v30, v30, v178, v100
	v_fma_f32 v31, v31, v178, v101
	s_nop 0
	s_nop 0
	v_pk_mul_f32 v[46:47], v[180:181], v[46:47] op_sel_hi:[0,1]
	v_mfma_f32_16x16x32_bf16 v[40:43], v[40:43], v[106:109], v[114:117]
	v_mul_f32_e64 v50, v180, v50
	v_mul_f32_e64 v51, v180, v51
	v_pk_mul_f32 v[54:55], v[180:181], v[54:55] op_sel_hi:[0,1]
	v_pk_mul_f32 v[44:45], v[180:181], v[44:45] op_sel_hi:[0,1]
	v_mfma_f32_16x16x32_bf16 v[56:59], v[60:63], v[106:109], v[114:117]
	v_mul_f32_e64 v48, v180, v48
	v_mul_f32_e64 v49, v180, v49
	s_nop 0
	v_pk_mul_f32 v[42:43], v[180:181], v[42:43] op_sel_hi:[0,1]
	v_pk_mul_f32 v[52:53], v[180:181], v[52:53] op_sel_hi:[0,1]
	v_mfma_f32_16x16x32_bf16 v[60:63], v[162:165], v[106:109], v[114:117]
	s_nop 0
	s_nop 0
	v_pk_mul_f32 v[58:59], v[180:181], v[58:59] op_sel_hi:[0,1]
	v_pk_mul_f32 v[40:41], v[180:181], v[40:41] op_sel_hi:[0,1]
	v_pk_mul_f32 v[56:57], v[180:181], v[56:57] op_sel_hi:[0,1]
	s_nop 0
	s_nop 1
	v_pk_mul_f32 v[62:63], v[180:181], v[62:63] op_sel_hi:[0,1]
	v_pk_mul_f32 v[60:61], v[180:181], v[60:61] op_sel_hi:[0,1]
	s_nop 0
	s_nop 0
	s_nop 0
	v_pk_fma_f32 v[24:25], v[24:25], v[178:179], v[60:61] op_sel_hi:[1,0,1]
	v_pk_fma_f32 v[20:21], v[20:21], v[178:179], v[56:57] op_sel_hi:[1,0,1]
	v_pk_fma_f32 v[16:17], v[16:17], v[178:179], v[40:41] op_sel_hi:[1,0,1]
	v_pk_fma_f32 v[12:13], v[12:13], v[178:179], v[52:53] op_sel_hi:[1,0,1]
	v_pk_fma_f32 v[8:9], v[8:9], v[178:179], v[48:49] op_sel_hi:[1,0,1]
	v_pk_fma_f32 v[4:5], v[4:5], v[178:179], v[44:45] op_sel_hi:[1,0,1]
	v_pk_fma_f32 v[26:27], v[26:27], v[178:179], v[62:63] op_sel_hi:[1,0,1]
	v_pk_fma_f32 v[22:23], v[22:23], v[178:179], v[58:59] op_sel_hi:[1,0,1]
	v_pk_fma_f32 v[18:19], v[18:19], v[178:179], v[42:43] op_sel_hi:[1,0,1]
	v_pk_fma_f32 v[14:15], v[14:15], v[178:179], v[54:55] op_sel_hi:[1,0,1]
	v_pk_fma_f32 v[10:11], v[10:11], v[178:179], v[50:51] op_sel_hi:[1,0,1]
	v_pk_fma_f32 v[6:7], v[6:7], v[178:179], v[46:47] op_sel_hi:[1,0,1]
	s_nop 0
	s_nop 0
	v_lshl_add_u64 v[32:33], s[14:15], 0, v[174:175]
	v_lshl_add_u64 v[34:35], s[14:15], 0, v[154:155]
	v_lshl_add_u64 v[32:33], v[32:33], 0, v[64:65]
	global_load_dwordx2 v[146:147], v[32:33], off nt
	global_load_dwordx2 v[148:149], v[32:33], off offset:512 nt
	global_load_dwordx4 v[150:153], v[34:35], off nt
	s_branch .Lm1_b1455

.Lm2_b1434:
	s_add_i32 s55, s51, -1
	s_min_u32 s14, s55, 60
	s_mul_i32 s14, s14, 0x8a00
	s_add_u32 s14, s4, s14
	s_addc_u32 s15, s5, 0
	s_add_u32 s16, s14, 0x19e00
	s_addc_u32 s17, s15, 0
	s_and_b64 vcc, exec, s[38:39]
	s_cbranch_vccnz .Lm2_b1438
	s_add_u32 s56, s16, s20
	s_addc_u32 s57, s17, s21
	v_lshl_add_u64 v[32:33], s[56:57], 0, v[154:155]
	global_load_dwordx4 v[82:85], v[32:33], off nt
	s_and_b64 vcc, exec, s[40:41]
	s_cbranch_vccz .Lm2_b1439

.Lm2_b1437:
	s_add_u32 s16, s16, s24
	s_addc_u32 s17, s17, s25
	v_lshl_add_u64 v[32:33], s[16:17], 0, v[154:155]
	global_load_dwordx4 v[90:93], v[32:33], off nt
	s_and_saveexec_b64 s[16:17], s[6:7]
	s_cbranch_execnz .Lm2_b1441
	s_branch .Lm2_b1442

.Lm2_b1439:
	s_add_u32 s56, s16, s22
	s_addc_u32 s57, s17, s23
	v_lshl_add_u64 v[32:33], s[56:57], 0, v[154:155]
	global_load_dwordx4 v[86:89], v[32:33], off nt
	s_and_b64 vcc, exec, s[42:43]
	s_cbranch_vccz .Lm2_b1437

.Lm2_b1441:
	v_lshl_add_u64 v[32:33], s[14:15], 0, v[154:155]
	v_add_co_u32_e32 v32, vcc, 0x22000, v32
	s_nop 1
	v_addc_co_u32_e32 v33, vcc, 0, v33, vcc
	global_load_dwordx4 v[94:97], v[32:33], off offset:1536 nt

.Lm2_b1453:
	v_add_u32_e32 v185, s16, v154
	ds_read_b128 v[44:47], v185 offset:16384
	ds_read_b128 v[48:51], v185 offset:17408
	ds_read_b128 v[52:55], v185
	ds_read_b128 v[56:59], v185 offset:1024
	ds_read_b128 v[60:63], v185 offset:2048
	ds_read_b128 v[102:105], v185 offset:3072
	ds_read_b128 v[110:113], v185 offset:4096
	ds_read_b128 v[142:145], v185 offset:5120
	ds_read_b128 v[162:165], v185 offset:6144
	ds_read_b128 v[186:189], v185 offset:7168
	s_min_u32 s14, s55, 61
	s_mul_i32 s14, s14, 0x8a00
	s_add_u32 s14, s4, s14
	s_addc_u32 s15, s5, 0
	v_cvt_pk_bf16_f32 v32, v0, v1
	v_cvt_pk_bf16_f32 v33, v2, v3
	v_cvt_pk_bf16_f32 v34, v4, v5
	v_cvt_pk_bf16_f32 v35, v6, v7
	v_cvt_pk_bf16_f32 v36, v8, v9
	v_cvt_pk_bf16_f32 v37, v10, v11
	v_cvt_pk_bf16_f32 v38, v12, v13
	v_cvt_pk_bf16_f32 v39, v14, v15
	v_cvt_pk_bf16_f32 v40, v16, v17
	v_cvt_pk_bf16_f32 v41, v18, v19
	v_cvt_pk_bf16_f32 v42, v20, v21
	v_cvt_pk_bf16_f32 v43, v22, v23
	v_cvt_pk_bf16_f32 v190, v24, v25
	v_cvt_pk_bf16_f32 v191, v26, v27
	v_cvt_pk_bf16_f32 v192, v28, v29
	v_cvt_pk_bf16_f32 v193, v30, v31
	s_waitcnt vmcnt(23) lgkmcnt(9)
	v_mfma_f32_16x16x32_bf16 v[138:141], v[44:47], v[200:203], v[114:117]
	s_add_u32 s14, s14, s19
	s_addc_u32 s15, s15, 0
	s_add_u32 s14, s14, 0x11400
	s_waitcnt lgkmcnt(7)
	v_mfma_f32_16x16x32_bf16 v[44:47], v[52:55], v[32:35], v[114:117]
	s_addc_u32 s15, s15, 0
	s_waitcnt lgkmcnt(3)
	v_mfma_f32_16x16x32_bf16 v[32:35], v[110:113], v[32:35], v[114:117]
	v_mfma_f32_16x16x32_bf16 v[44:47], v[56:59], v[36:39], v[44:47]
	s_waitcnt lgkmcnt(2)
	v_mfma_f32_16x16x32_bf16 v[32:35], v[142:145], v[36:39], v[32:35]
	v_mfma_f32_16x16x32_bf16 v[36:39], v[60:63], v[40:43], v[44:47]
	s_nop 4
	s_nop 0
	s_nop 0
	s_waitcnt lgkmcnt(1)
	v_mfma_f32_16x16x32_bf16 v[40:43], v[162:165], v[40:43], v[32:35]
	s_nop 2
	s_nop 0
	s_nop 0
	v_mfma_f32_16x16x32_bf16 v[142:145], v[102:105], v[190:193], v[36:39]
	s_nop 2
	ds_read_b128 v[36:39], v185 offset:8192
	ds_read_b128 v[44:47], v185 offset:9216
	ds_read_b128 v[52:55], v185 offset:10240
	ds_read_b128 v[56:59], v185 offset:11264
	s_waitcnt lgkmcnt(4)
	v_mfma_f32_16x16x32_bf16 v[102:105], v[186:189], v[190:193], v[40:43]
	s_nop 2
	ds_read_b128 v[40:43], v185 offset:12288
	ds_read_b128 v[60:63], v185 offset:13312
	ds_read_b128 v[162:165], v185 offset:14336
	ds_read_b128 v[186:189], v185 offset:15360
	v_mfma_f32_16x16x32_bf16 v[110:113], v[48:51], v[200:203], v[114:117]
	s_waitcnt lgkmcnt(7)
	v_mfma_f32_16x16x32_bf16 v[36:39], v[36:39], v[204:207], v[114:117]
	s_waitcnt lgkmcnt(0)
	v_mfma_f32_16x16x32_bf16 v[200:203], v[186:189], v[204:207], v[114:117]
	v_mfma_f32_16x16x32_bf16 v[44:47], v[44:47], v[204:207], v[114:117]
	s_nop 4
	v_mul_f32_e64 v36, v180, v36
	v_mul_f32_e64 v37, v180, v37
	v_pk_mul_f32 v[38:39], v[180:181], v[38:39] op_sel_hi:[0,1]
	v_pk_fma_f32 v[0:1], v[0:1], v[178:179], v[36:37] op_sel_hi:[1,0,1]
	s_nop 0
	v_pk_fma_f32 v[2:3], v[2:3], v[178:179], v[38:39] op_sel_hi:[1,0,1]
	s_nop 0
	v_mfma_f32_16x16x32_bf16 v[48:51], v[52:55], v[204:207], v[114:117]
	v_mul_f32_e64 v202, v180, v202
	v_mul_f32_e64 v203, v180, v203
	v_pk_mul_f32 v[200:201], v[180:181], v[200:201] op_sel_hi:[0,1]
	v_pk_fma_f32 v[28:29], v[28:29], v[178:179], v[200:201] op_sel_hi:[1,0,1]
	v_mfma_f32_16x16x32_bf16 v[52:55], v[56:59], v[204:207], v[114:117]
	v_fma_f32 v30, v30, v178, v202
	v_fma_f32 v31, v31, v178, v203
	s_nop 0
	s_nop 0
	v_pk_mul_f32 v[46:47], v[180:181], v[46:47] op_sel_hi:[0,1]
	v_mfma_f32_16x16x32_bf16 v[40:43], v[40:43], v[204:207], v[114:117]
	v_mul_f32_e64 v50, v180, v50
	v_mul_f32_e64 v51, v180, v51
	v_pk_mul_f32 v[54:55], v[180:181], v[54:55] op_sel_hi:[0,1]
	v_pk_mul_f32 v[44:45], v[180:181], v[44:45] op_sel_hi:[0,1]
	v_mfma_f32_16x16x32_bf16 v[56:59], v[60:63], v[204:207], v[114:117]
	v_mul_f32_e64 v48, v180, v48
	v_mul_f32_e64 v49, v180, v49
	s_nop 0
	v_pk_mul_f32 v[42:43], v[180:181], v[42:43] op_sel_hi:[0,1]
	v_pk_mul_f32 v[52:53], v[180:181], v[52:53] op_sel_hi:[0,1]
	v_mfma_f32_16x16x32_bf16 v[60:63], v[162:165], v[204:207], v[114:117]
	s_nop 0
	s_nop 0
	v_pk_mul_f32 v[58:59], v[180:181], v[58:59] op_sel_hi:[0,1]
	v_pk_mul_f32 v[40:41], v[180:181], v[40:41] op_sel_hi:[0,1]
	v_pk_mul_f32 v[56:57], v[180:181], v[56:57] op_sel_hi:[0,1]
	s_nop 0
	s_nop 1
	v_pk_mul_f32 v[62:63], v[180:181], v[62:63] op_sel_hi:[0,1]
	v_pk_mul_f32 v[60:61], v[180:181], v[60:61] op_sel_hi:[0,1]
	s_nop 0
	s_nop 0
	s_nop 0
	v_pk_fma_f32 v[24:25], v[24:25], v[178:179], v[60:61] op_sel_hi:[1,0,1]
	v_pk_fma_f32 v[20:21], v[20:21], v[178:179], v[56:57] op_sel_hi:[1,0,1]
	v_pk_fma_f32 v[16:17], v[16:17], v[178:179], v[40:41] op_sel_hi:[1,0,1]
	v_pk_fma_f32 v[12:13], v[12:13], v[178:179], v[52:53] op_sel_hi:[1,0,1]
	v_pk_fma_f32 v[8:9], v[8:9], v[178:179], v[48:49] op_sel_hi:[1,0,1]
	v_pk_fma_f32 v[4:5], v[4:5], v[178:179], v[44:45] op_sel_hi:[1,0,1]
	v_pk_fma_f32 v[26:27], v[26:27], v[178:179], v[62:63] op_sel_hi:[1,0,1]
	v_pk_fma_f32 v[22:23], v[22:23], v[178:179], v[58:59] op_sel_hi:[1,0,1]
	v_pk_fma_f32 v[18:19], v[18:19], v[178:179], v[42:43] op_sel_hi:[1,0,1]
	v_pk_fma_f32 v[14:15], v[14:15], v[178:179], v[54:55] op_sel_hi:[1,0,1]
	v_pk_fma_f32 v[10:11], v[10:11], v[178:179], v[50:51] op_sel_hi:[1,0,1]
	v_pk_fma_f32 v[6:7], v[6:7], v[178:179], v[46:47] op_sel_hi:[1,0,1]
	s_nop 0
	s_nop 0
	v_lshl_add_u64 v[32:33], s[14:15], 0, v[174:175]
	v_lshl_add_u64 v[34:35], s[14:15], 0, v[154:155]
	v_lshl_add_u64 v[32:33], v[32:33], 0, v[64:65]
	global_load_dwordx2 v[98:99], v[32:33], off nt
	global_load_dwordx2 v[100:101], v[32:33], off offset:512 nt
	global_load_dwordx4 v[106:109], v[34:35], off nt
	s_branch .Lm2_b1455

.LBB0_1466:
	s_lshl_b32 s12, s82, 10
	s_addk_i32 s12, 0x2000
	s_ashr_i32 s13, s12, 31
	s_add_u32 s12, s10, s12
	s_addc_u32 s13, s11, s13
	v_lshl_add_u64 v[0:1], s[12:13], 0, v[154:155]
	global_load_dwordx4 v[86:89], v[0:1], off nt
	s_and_b64 vcc, exec, s[42:43]
	s_cbranch_vccz .LBB0_1430
	s_branch .LBB0_1431

.LBB0_1471:
	s_mul_i32 s5, s18, 0x228000
	s_mul_hi_i32 s4, s18, 0x228000
	s_waitcnt lgkmcnt(0)
	s_add_u32 s5, s48, s5
	s_addc_u32 s6, s49, s4
	s_add_u32 s4, s5, 0xafa00000
	s_addc_u32 s5, s6, 0
	s_cmp_lt_i32 s82, 18
	s_cselect_b64 s[10:11], -1, 0
	s_cmp_gt_i32 s82, 17
	s_waitcnt vmcnt(0)
	v_lshlrev_b32_e32 v98, 4, v227
	s_cbranch_scc1 .LBB0_1473
	s_lshl_b32 s6, s82, 10
	s_ashr_i32 s7, s6, 31
	s_add_u32 s6, s4, s6
	v_lshlrev_b32_e32 v0, 4, v227
	s_addc_u32 s7, s5, s7
	v_ashrrev_i32_e32 v1, 31, v0
	v_lshl_add_u64 v[0:1], s[6:7], 0, v[0:1]
	global_load_dwordx4 v[0:3], v[0:1], off nt
.LBB0_1473:
	s_cmp_lt_i32 s82, 10
	s_cselect_b64 s[12:13], -1, 0
	s_cmp_gt_i32 s82, 9
	s_cbranch_scc1 .LBB0_1475
	s_lshl_b32 s6, s82, 10
	s_addk_i32 s6, 0x2000
	s_ashr_i32 s7, s6, 31
	s_add_u32 s6, s4, s6
	v_lshlrev_b32_e32 v4, 4, v227
	s_addc_u32 s7, s5, s7
	v_ashrrev_i32_e32 v5, 31, v4
	v_lshl_add_u64 v[4:5], s[6:7], 0, v[4:5]
	global_load_dwordx4 v[4:7], v[4:5], off nt
.LBB0_1475:
	s_cmp_lt_i32 s82, 2
	s_cselect_b64 s[14:15], -1, 0
	s_cmp_gt_i32 s82, 1
	s_cbranch_scc1 .LBB0_1477
	s_lshl_b32 s6, s82, 10
	s_addk_i32 s6, 0x4000
	s_ashr_i32 s7, s6, 31
	s_add_u32 s6, s4, s6
	v_lshlrev_b32_e32 v8, 4, v227
	s_addc_u32 s7, s5, s7
	v_ashrrev_i32_e32 v9, 31, v8
	v_lshl_add_u64 v[8:9], s[6:7], 0, v[8:9]
	global_load_dwordx4 v[8:11], v[8:9], off nt
.LBB0_1477:
	s_cmp_eq_u32 s82, 7
	s_cselect_b64 s[6:7], -1, 0
	v_cmp_gt_i32_e32 vcc, 32, v227
	s_and_b64 s[6:7], s[6:7], vcc
	s_xor_b64 s[8:9], s[6:7], -1
	s_and_saveexec_b64 s[16:17], s[8:9]
	s_xor_b64 s[16:17], exec, s[16:17]
	v_lshlrev_b32_e32 v98, 4, v227
	s_or_saveexec_b64 s[16:17], s[16:17]
	s_xor_b64 exec, exec, s[16:17]
	s_cbranch_execz .LBB0_1481
	v_ashrrev_i32_e32 v99, 31, v98
	v_lshl_add_u64 v[12:13], s[4:5], 0, v[98:99]
	v_add_co_u32_e32 v12, vcc, 0x8000, v12
	s_nop 1
	v_addc_co_u32_e32 v13, vcc, 0, v13, vcc
	global_load_dwordx4 v[12:15], v[12:13], off offset:2048 nt

.LBB0_1489:
	s_or_b64 exec, exec, s[10:11]
	s_add_u32 s12, s4, 0x8a00
	s_addc_u32 s13, s5, 0
	s_and_b64 vcc, exec, s[38:39]
	v_ashrrev_i32_e32 v99, 31, v98
	s_cbranch_vccnz .LBB0_1493
	s_lshl_b32 s10, s82, 10
	s_ashr_i32 s11, s10, 31
	s_add_u32 s10, s12, s10
	s_addc_u32 s11, s13, s11
	s_waitcnt vmcnt(0)
	v_lshl_add_u64 v[0:1], s[10:11], 0, v[98:99]
	global_load_dwordx4 v[0:3], v[0:1], off nt
	s_and_b64 vcc, exec, s[40:41]
	s_cbranch_vccz .LBB0_1494

.LBB0_1492:
	s_lshl_b32 s10, s82, 10
	s_addk_i32 s10, 0x4000
	s_ashr_i32 s11, s10, 31
	s_add_u32 s10, s12, s10
	s_addc_u32 s11, s13, s11
	s_waitcnt vmcnt(0)
	v_lshl_add_u64 v[8:9], s[10:11], 0, v[98:99]
	global_load_dwordx4 v[8:11], v[8:9], off nt
	s_and_saveexec_b64 s[10:11], s[6:7]
	s_cbranch_execnz .LBB0_1496
	s_branch .LBB0_1497

.LBB0_1494:
	s_lshl_b32 s10, s82, 10
	s_addk_i32 s10, 0x2000
	s_ashr_i32 s11, s10, 31
	s_add_u32 s10, s12, s10
	s_addc_u32 s11, s13, s11
	s_waitcnt vmcnt(0)
	v_lshl_add_u64 v[4:5], s[10:11], 0, v[98:99]
	global_load_dwordx4 v[4:7], v[4:5], off nt
	s_and_b64 vcc, exec, s[42:43]
	s_cbranch_vccz .LBB0_1492

.LBB0_1496:
	s_waitcnt vmcnt(0)
	v_lshl_add_u64 v[12:13], s[4:5], 0, v[98:99]
	v_add_co_u32_e32 v12, vcc, 0x11000, v12
	s_nop 1
	v_addc_co_u32_e32 v13, vcc, 0, v13, vcc
	global_load_dwordx4 v[12:15], v[12:13], off offset:512 nt
.LBB0_1497:
	s_or_b64 exec, exec, s[10:11]
	s_add_u32 s10, s4, 0x11400
	s_addc_u32 s11, s5, 0
	s_and_b64 vcc, exec, s[38:39]
	s_cbranch_vccnz .LBB0_1521
	s_lshl_b32 s14, s82, 10
	s_ashr_i32 s15, s14, 31
	s_add_u32 s14, s10, s14
	s_addc_u32 s15, s11, s15
	v_lshl_add_u64 v[16:17], s[14:15], 0, v[98:99]
	global_load_dwordx4 v[16:19], v[16:17], off nt
	s_and_b64 vcc, exec, s[40:41]
	s_cbranch_vccz .LBB0_1522

.LBB0_1500:
	s_lshl_b32 s14, s82, 10
	s_addk_i32 s14, 0x4000
	s_ashr_i32 s15, s14, 31
	s_add_u32 s10, s10, s14
	s_addc_u32 s11, s11, s15
	v_lshl_add_u64 v[24:25], s[10:11], 0, v[98:99]
	global_load_dwordx4 v[24:27], v[24:25], off nt
.LBB0_1501:
	s_and_saveexec_b64 s[10:11], s[8:9]
	s_xor_b64 s[8:9], exec, s[10:11]
	s_or_saveexec_b64 s[8:9], s[8:9]
	s_xor_b64 exec, exec, s[8:9]
	s_cbranch_execz .LBB0_1503
	v_lshl_add_u64 v[28:29], s[4:5], 0, v[98:99]
	v_add_co_u32_e32 v28, vcc, 0x19000, v28
	s_nop 1
	v_addc_co_u32_e32 v29, vcc, 0, v29, vcc
	global_load_dwordx4 v[28:31], v[28:29], off offset:3072 nt
.LBB0_1503:
	s_or_b64 exec, exec, s[8:9]
	s_ashr_i32 s8, s18, 2
	v_ashrrev_i32_e32 v41, 4, v227
	s_lshl_b32 s10, s82, 11
	s_ashr_i32 s9, s8, 31
	v_and_b32_e32 v40, 15, v227
	s_add_i32 s14, s10, 0x4c00
	v_lshlrev_b32_e32 v34, 3, v41
	s_mov_b32 s16, 0xffffff0
	s_lshl_b64 s[8:9], s[8:9], 21
	s_ashr_i32 s15, s14, 31
	v_and_or_b32 v32, v34, s16, v40
	s_add_u32 s10, s4, s14
	v_lshlrev_b32_e32 v100, 4, v32
	s_addc_u32 s11, s5, s15
	v_ashrrev_i32_e32 v101, 31, v100
	v_lshl_add_u64 v[32:33], s[10:11], 0, v[100:101]
	v_and_b32_e32 v64, 8, v34
	v_lshl_add_u64 v[32:33], v[32:33], 0, v[64:65]
	global_load_dwordx2 v[94:95], v[32:33], off nt
	global_load_dwordx2 v[96:97], v[32:33], off offset:512 nt
	v_lshl_add_u64 v[32:33], s[10:11], 0, v[98:99]
	s_add_u32 s10, s12, s14
	s_addc_u32 s11, s13, s15
	v_lshl_add_u64 v[34:35], s[10:11], 0, v[100:101]
	v_lshl_add_u64 v[34:35], v[34:35], 0, v[64:65]
	global_load_dwordx4 v[52:55], v[32:33], off nt
	global_load_dwordx2 v[102:103], v[34:35], off nt
	v_lshl_add_u64 v[32:33], s[10:11], 0, v[98:99]
	global_load_dwordx2 v[104:105], v[34:35], off offset:512 nt
	s_nop 0
	global_load_dwordx4 v[32:35], v[32:33], off nt
	s_lshl_b32 s10, s82, 4
	s_lshl_b32 s16, s82, 10
	s_and_b32 s12, s18, 3
	s_ashr_i32 s11, s10, 31
	s_add_i32 s19, s16, 0x2000
	s_add_i32 s21, s16, 0x4000
	s_lshl_b32 s12, s12, 8
	s_ashr_i32 s17, s16, 31
	s_ashr_i32 s20, s19, 31
	s_ashr_i32 s22, s21, 31
	s_or_b32 s8, s8, s12
	s_lshl_b64 s[10:11], s[10:11], 1
	s_add_u32 s8, s8, s10
	s_addc_u32 s9, s9, s11
	s_add_u32 s8, s48, s8
	v_lshl_or_b32 v40, v41, 11, v40
	v_mov_b32_e32 v41, v65
	s_addc_u32 s9, s49, s9
	v_lshl_add_u64 v[42:43], v[40:41], 1, s[8:9]
	s_mov_b64 s[10:11], 0x74200800
	s_add_u32 s8, s8, 0x74200000
	v_lshl_add_u64 v[106:107], v[42:43], 0, s[10:11]
	v_add_u32_e32 v42, 0x2600, v40
	v_mov_b32_e32 v43, v65
	s_addc_u32 s9, s9, 0
	v_lshl_add_u64 v[108:109], v[42:43], 1, s[8:9]
	v_add_u32_e32 v42, 0x2400, v40
	v_lshl_add_u64 v[110:111], v[42:43], 1, s[8:9]
	v_add_u32_e32 v42, 0x2000, v40
	v_add_u32_e32 v40, 0x2200, v40
	v_mov_b32_e32 v36, v65
	v_lshl_add_u64 v[114:115], v[40:41], 1, s[8:9]
	v_mov_b32_e32 v40, 0
	s_waitcnt vmcnt(0) lgkmcnt(0)
	s_barrier
	v_and_b32_e32 v121, -16, v227
	v_mov_b32_e32 v37, v36
	v_mov_b32_e32 v38, v36
	v_mov_b32_e32 v39, v36
	s_mov_b32 s18, 1
	v_lshl_add_u64 v[112:113], v[42:43], 1, s[8:9]
	s_mov_b64 s[8:9], 0
	v_mov_b32_e32 v41, v40
	v_mov_b32_e32 v42, v40
	v_mov_b32_e32 v43, v40
	v_mov_b32_e32 v60, v40
	v_mov_b32_e32 v61, v40
	v_mov_b32_e32 v62, v40
	v_mov_b32_e32 v63, v40
	v_mov_b32_e32 v66, v40
	v_mov_b32_e32 v67, v40
	v_mov_b32_e32 v68, v40
	v_mov_b32_e32 v69, v40
	v_mov_b32_e32 v70, v40
	v_mov_b32_e32 v71, v40
	v_mov_b32_e32 v72, v40
	v_mov_b32_e32 v73, v40
	v_mov_b32_e32 v74, v40
	v_mov_b32_e32 v75, v40
	v_mov_b32_e32 v76, v40
	v_mov_b32_e32 v77, v40
	v_mov_b32_e32 v78, v40
	v_mov_b32_e32 v79, v40
	v_mov_b32_e32 v80, v40
	v_mov_b32_e32 v81, v40
	v_mov_b32_e32 v82, v40
	v_mov_b32_e32 v83, v40
	v_mov_b32_e32 v84, v40
	v_mov_b32_e32 v85, v40
	v_mov_b32_e32 v86, v40
	v_mov_b32_e32 v87, v40
	v_mov_b32_e32 v88, v40
	v_mov_b32_e32 v89, v40
	s_branch .LBB0_1505
.LBB0_1505:
	s_add_i32 s23, s18, -1
	s_min_u32 s10, s23, 60
	s_mul_i32 s10, s10, 0x8a00
	s_add_u32 s10, s4, s10
	s_addc_u32 s11, s5, 0
	s_add_u32 s12, s10, 0x19e00
	s_addc_u32 s13, s11, 0
	s_and_b64 vcc, exec, s[38:39]
	s_cbranch_vccnz .LBB0_1509
	s_add_u32 s24, s12, s16
	s_addc_u32 s25, s13, s17
	v_lshl_add_u64 v[90:91], s[24:25], 0, v[98:99]
	global_load_dwordx4 v[90:93], v[90:91], off nt
	s_and_b64 vcc, exec, s[40:41]
	s_cbranch_vccz .LBB0_1510

.LBB0_1508:
	s_add_u32 s12, s12, s21
	s_addc_u32 s13, s13, s22
	v_lshl_add_u64 v[48:49], s[12:13], 0, v[98:99]
	global_load_dwordx4 v[48:51], v[48:49], off nt
	s_and_saveexec_b64 s[12:13], s[6:7]
	s_cbranch_execnz .LBB0_1512
	s_branch .LBB0_1513

.LBB0_1510:
	s_add_u32 s24, s12, s19
	s_addc_u32 s25, s13, s20
	v_lshl_add_u64 v[44:45], s[24:25], 0, v[98:99]
	global_load_dwordx4 v[44:47], v[44:45], off nt
	s_and_b64 vcc, exec, s[42:43]
	s_cbranch_vccz .LBB0_1508

.LBB0_1512:
	v_lshl_add_u64 v[56:57], s[10:11], 0, v[98:99]
	v_add_co_u32_e32 v56, vcc, 0x22000, v56
	s_nop 1
	v_addc_co_u32_e32 v57, vcc, 0, v57, vcc
	global_load_dwordx4 v[56:59], v[56:57], off offset:1536 nt
.LBB0_1513:
	s_or_b64 exec, exec, s[12:13]
	s_min_u32 s10, s23, 61
	s_mul_i32 s10, s10, 0x8a00
	s_add_u32 s10, s4, s10
	s_addc_u32 s11, s5, 0
	s_bitcmp1_b32 s23, 0
	s_cselect_b32 s12, 0x4a00, 0
	s_add_i32 s12, s12, 0
	v_add_u32_e32 v162, s12, v98
	ds_read_b128 v[122:125], v162
	ds_read_b128 v[126:129], v162 offset:1024
	ds_read_b128 v[130:133], v162 offset:2048
	ds_read_b128 v[134:137], v162 offset:3072
	ds_read_b128 v[116:119], v162 offset:4096
	ds_read_b128 v[138:141], v162 offset:5120
	ds_read_b128 v[142:145], v162 offset:6144
	ds_read_b128 v[146:149], v162 offset:7168
	ds_read_b128 v[150:153], v162 offset:8192
	ds_read_b128 v[154:157], v162 offset:9216
	ds_read_b128 v[158:161], v162 offset:10240
	ds_read_b128 v[172:175], v162 offset:11264
	ds_read_b128 v[176:179], v162 offset:12288
	ds_read_b128 v[180:183], v162 offset:13312
	ds_read_b128 v[184:187], v162 offset:14336
	ds_read_b128 v[188:191], v162 offset:15360
	ds_read_b128 v[192:195], v162 offset:16384
	ds_read_b128 v[196:199], v162 offset:17408
	v_add_u32_e32 v162, s12, v121
	ds_read_b128 v[200:203], v162 offset:18432
	ds_read_b128 v[204:207], v162 offset:18496
	ds_read_b128 v[208:211], v162 offset:18560
	ds_read_b128 v[230:233], v162 offset:18624
	ds_read_b128 v[234:237], v162 offset:18688
	ds_read_b128 v[238:241], v162 offset:18752
	ds_read_b128 v[242:245], v162 offset:18816
	ds_read_b128 v[246:249], v162 offset:18880
	s_waitcnt vmcnt(23) lgkmcnt(9)
	v_mfma_f32_16x16x32_bf16 v[192:195], v[192:195], v[94:97], 0
	v_cvt_pk_bf16_f32 v162, v40, v41
	v_cvt_pk_bf16_f32 v163, v42, v43
	v_cvt_pk_bf16_f32 v164, v60, v61
	s_waitcnt lgkmcnt(8)
	v_mfma_f32_16x16x32_bf16 v[94:97], v[196:199], v[94:97], 0
	v_cvt_pk_bf16_f32 v165, v62, v63
	v_cvt_pk_bf16_f32 v196, v66, v67
	v_cvt_pk_bf16_f32 v197, v68, v69
	v_mfma_f32_16x16x32_bf16 v[94:97], v[116:119], v[162:165], v[94:97]
	v_cvt_pk_bf16_f32 v198, v70, v71
	v_cvt_pk_bf16_f32 v199, v72, v73
	v_cvt_pk_bf16_f32 v220, v74, v75
	v_cvt_pk_bf16_f32 v221, v76, v77
	v_mfma_f32_16x16x32_bf16 v[94:97], v[138:141], v[196:199], v[94:97]
	v_cvt_pk_bf16_f32 v222, v78, v79
	v_cvt_pk_bf16_f32 v223, v80, v81
	s_add_u32 s10, s10, s14
	s_addc_u32 s11, s11, s15
	v_mfma_f32_16x16x32_bf16 v[94:97], v[142:145], v[220:223], v[94:97]
	s_add_u32 s10, s10, 0x11400
	v_cvt_pk_bf16_f32 v138, v82, v83
	v_cvt_pk_bf16_f32 v139, v84, v85
	v_cvt_pk_bf16_f32 v140, v86, v87
	v_cvt_pk_bf16_f32 v141, v88, v89
	s_addc_u32 s11, s11, 0
	v_mfma_f32_16x16x32_bf16 v[122:125], v[122:125], v[162:165], v[192:195]
	s_waitcnt lgkmcnt(7)
	v_pk_mul_f32 v[42:43], v[42:43], v[202:203]
	v_pk_mul_f32 v[40:41], v[40:41], v[200:201]
	s_waitcnt lgkmcnt(6)
	v_pk_mul_f32 v[62:63], v[62:63], v[206:207]
	v_mfma_f32_16x16x32_bf16 v[142:145], v[146:149], v[138:141], v[94:97]
	v_mul_f32_e64 v60, v60, v204
	v_mul_f32_e64 v61, v61, v205
	s_waitcnt lgkmcnt(5)
	v_pk_mul_f32 v[68:69], v[68:69], v[210:211]
	v_pk_mul_f32 v[66:67], v[66:67], v[208:209]
	v_lshl_add_u64 v[94:95], s[10:11], 0, v[100:101]
	v_lshl_add_u64 v[94:95], v[94:95], 0, v[64:65]
	global_load_dwordx2 v[36:37], v[94:95], off nt
	global_load_dwordx2 v[38:39], v[94:95], off offset:512 nt
	v_lshl_add_u64 v[94:95], s[10:11], 0, v[98:99]
	global_load_dwordx4 v[108:111], v[94:95], off nt
	v_mfma_f32_16x16x32_bf16 v[122:125], v[126:129], v[196:199], v[122:125]
	s_waitcnt lgkmcnt(4)
	v_pk_mul_f32 v[72:73], v[72:73], v[232:233]
	v_pk_mul_f32 v[70:71], v[70:71], v[230:231]
	s_waitcnt lgkmcnt(3)
	v_pk_mul_f32 v[76:77], v[76:77], v[236:237]
	v_mfma_f32_16x16x32_bf16 v[122:125], v[130:133], v[220:223], v[122:125]
	v_mul_f32_e64 v74, v74, v234
	v_mul_f32_e64 v75, v75, v235
	s_waitcnt lgkmcnt(2)
	v_pk_mul_f32 v[80:81], v[80:81], v[240:241]
	v_pk_mul_f32 v[78:79], v[78:79], v[238:239]
	v_mfma_f32_16x16x32_bf16 v[122:125], v[134:137], v[138:141], v[122:125]
	s_waitcnt lgkmcnt(1)
	v_pk_mul_f32 v[84:85], v[84:85], v[244:245]
	v_pk_mul_f32 v[82:83], v[82:83], v[242:243]
	s_waitcnt lgkmcnt(0)
	v_pk_mul_f32 v[88:89], v[88:89], v[248:249]
	v_pk_mul_f32 v[86:87], v[86:87], v[246:247]
	v_lshl_add_u64 v[128:129], v[112:113], 0, s[8:9]
	s_nop 0
	v_bfe_u32 v126, v122, 16, 1
	v_add3_u32 v122, v122, v126, s30
	v_lshl_add_u64 v[126:127], v[106:107], 0, s[8:9]
	global_store_short_d16_hi v[126:127], v122, off offset:-2048
	v_bfe_u32 v122, v142, 16, 1
	v_add3_u32 v122, v142, v122, s30
	s_nop 0
	v_mfma_f32_16x16x32_bf16 v[40:43], v[150:153], v[52:55], v[40:43]
	global_store_short_d16_hi v[128:129], v122, off
	v_bfe_u32 v122, v123, 16, 1
	v_add3_u32 v122, v123, v122, s30
	v_mfma_f32_16x16x32_bf16 v[60:63], v[154:157], v[52:55], v[60:63]
	global_store_short_d16_hi v[126:127], v122, off offset:-1024
	s_bitcmp1_b32 s18, 0
	s_cselect_b32 s10, 0x4a00, 0
	v_mfma_f32_16x16x32_bf16 v[66:69], v[158:161], v[52:55], v[66:69]
	s_and_b64 vcc, exec, s[38:39]
	v_mfma_f32_16x16x32_bf16 v[70:73], v[172:175], v[52:55], v[70:73]
	v_mfma_f32_16x16x32_bf16 v[74:77], v[176:179], v[52:55], v[74:77]
	v_mfma_f32_16x16x32_bf16 v[78:81], v[180:183], v[52:55], v[78:81]
	v_mfma_f32_16x16x32_bf16 v[82:85], v[184:187], v[52:55], v[82:85]
	v_mfma_f32_16x16x32_bf16 v[86:89], v[188:191], v[52:55], v[86:89]
	v_bfe_u32 v52, v143, 16, 1
	v_add3_u32 v54, v143, v52, s30
	v_lshl_add_u64 v[52:53], v[112:113], 0, s[8:9]
	global_store_short_d16_hi v[52:53], v54, off offset:1024
	v_bfe_u32 v52, v124, 16, 1
	v_add3_u32 v52, v124, v52, s30
	global_store_short_d16_hi v[126:127], v52, off
	v_bfe_u32 v52, v144, 16, 1
	v_add3_u32 v54, v144, v52, s30
	v_lshl_add_u64 v[52:53], v[112:113], 0, s[8:9]
	global_store_short_d16_hi v[52:53], v54, off offset:2048
	v_bfe_u32 v52, v125, 16, 1
	v_add3_u32 v52, v125, v52, s30
	global_store_short_d16_hi v[126:127], v52, off offset:1024
	v_bfe_u32 v52, v145, 16, 1
	v_add3_u32 v54, v145, v52, s30
	v_lshl_add_u64 v[52:53], v[112:113], 0, s[8:9]
	global_store_short_d16_hi v[52:53], v54, off offset:3072
	v_add_u32_e32 v52, s10, v120
	v_add_u32_e32 v53, s16, v52
	s_waitcnt vmcnt(37)
	s_cbranch_vccnz .LBB0_1517
	ds_write_b128 v53, v[0:3]
	s_and_b64 vcc, exec, s[40:41]
	s_cbranch_vccz .LBB0_1518

.Lh1_b1505:
	s_add_i32 s23, s18, -1
	s_min_u32 s10, s23, 60
	s_mul_i32 s10, s10, 0x8a00
	s_add_u32 s10, s4, s10
	s_addc_u32 s11, s5, 0
	s_add_u32 s12, s10, 0x19e00
	s_addc_u32 s13, s11, 0
	s_and_b64 vcc, exec, s[38:39]
	s_cbranch_vccnz .Lh1_b1509
	s_add_u32 s24, s12, s16
	s_addc_u32 s25, s13, s17
	v_lshl_add_u64 v[0:1], s[24:25], 0, v[98:99]
	global_load_dwordx4 v[0:3], v[0:1], off nt
	s_and_b64 vcc, exec, s[40:41]
	s_cbranch_vccz .Lh1_b1510

.Lh1_b1508:
	s_add_u32 s12, s12, s21
	s_addc_u32 s13, s13, s22
	v_lshl_add_u64 v[8:9], s[12:13], 0, v[98:99]
	global_load_dwordx4 v[8:11], v[8:9], off nt
	s_and_saveexec_b64 s[12:13], s[6:7]
	s_cbranch_execnz .Lh1_b1512
	s_branch .Lh1_b1513

.Lh1_b1510:
	s_add_u32 s24, s12, s19
	s_addc_u32 s25, s13, s20
	v_lshl_add_u64 v[4:5], s[24:25], 0, v[98:99]
	global_load_dwordx4 v[4:7], v[4:5], off nt
	s_and_b64 vcc, exec, s[42:43]
	s_cbranch_vccz .Lh1_b1508

.Lh1_b1512:
	v_lshl_add_u64 v[12:13], s[10:11], 0, v[98:99]
	v_add_co_u32_e32 v12, vcc, 0x22000, v12
	s_nop 1
	v_addc_co_u32_e32 v13, vcc, 0, v13, vcc
	global_load_dwordx4 v[12:15], v[12:13], off offset:1536 nt
.Lh1_b1513:
	s_or_b64 exec, exec, s[12:13]
	s_min_u32 s10, s23, 61
	s_mul_i32 s10, s10, 0x8a00
	s_add_u32 s10, s4, s10
	s_addc_u32 s11, s5, 0
	s_bitcmp1_b32 s23, 0
	s_cselect_b32 s12, 0x4a00, 0
	s_add_i32 s12, s12, 0
	v_add_u32_e32 v162, s12, v98
	ds_read_b128 v[122:125], v162
	ds_read_b128 v[126:129], v162 offset:1024
	ds_read_b128 v[130:133], v162 offset:2048
	ds_read_b128 v[134:137], v162 offset:3072
	ds_read_b128 v[116:119], v162 offset:4096
	ds_read_b128 v[138:141], v162 offset:5120
	ds_read_b128 v[142:145], v162 offset:6144
	ds_read_b128 v[146:149], v162 offset:7168
	ds_read_b128 v[150:153], v162 offset:8192
	ds_read_b128 v[154:157], v162 offset:9216
	ds_read_b128 v[158:161], v162 offset:10240
	ds_read_b128 v[172:175], v162 offset:11264
	ds_read_b128 v[176:179], v162 offset:12288
	ds_read_b128 v[180:183], v162 offset:13312
	ds_read_b128 v[184:187], v162 offset:14336
	ds_read_b128 v[188:191], v162 offset:15360
	ds_read_b128 v[192:195], v162 offset:16384
	ds_read_b128 v[196:199], v162 offset:17408
	v_add_u32_e32 v162, s12, v121
	ds_read_b128 v[200:203], v162 offset:18432
	ds_read_b128 v[204:207], v162 offset:18496
	ds_read_b128 v[208:211], v162 offset:18560
	ds_read_b128 v[230:233], v162 offset:18624
	ds_read_b128 v[234:237], v162 offset:18688
	ds_read_b128 v[238:241], v162 offset:18752
	ds_read_b128 v[242:245], v162 offset:18816
	ds_read_b128 v[246:249], v162 offset:18880
	s_waitcnt vmcnt(23) lgkmcnt(9)
	v_mfma_f32_16x16x32_bf16 v[192:195], v[192:195], v[102:105], 0
	v_cvt_pk_bf16_f32 v162, v40, v41
	v_cvt_pk_bf16_f32 v163, v42, v43
	v_cvt_pk_bf16_f32 v164, v60, v61
	s_waitcnt lgkmcnt(8)
	v_mfma_f32_16x16x32_bf16 v[102:105], v[196:199], v[102:105], 0
	v_cvt_pk_bf16_f32 v165, v62, v63
	v_cvt_pk_bf16_f32 v196, v66, v67
	v_cvt_pk_bf16_f32 v197, v68, v69
	v_mfma_f32_16x16x32_bf16 v[102:105], v[116:119], v[162:165], v[102:105]
	v_cvt_pk_bf16_f32 v198, v70, v71
	v_cvt_pk_bf16_f32 v199, v72, v73
	v_cvt_pk_bf16_f32 v220, v74, v75
	v_cvt_pk_bf16_f32 v221, v76, v77
	v_mfma_f32_16x16x32_bf16 v[102:105], v[138:141], v[196:199], v[102:105]
	v_cvt_pk_bf16_f32 v222, v78, v79
	v_cvt_pk_bf16_f32 v223, v80, v81
	s_add_u32 s10, s10, s14
	s_addc_u32 s11, s11, s15
	v_mfma_f32_16x16x32_bf16 v[102:105], v[142:145], v[220:223], v[102:105]
	s_add_u32 s10, s10, 0x11400
	v_cvt_pk_bf16_f32 v138, v82, v83
	v_cvt_pk_bf16_f32 v139, v84, v85
	v_cvt_pk_bf16_f32 v140, v86, v87
	v_cvt_pk_bf16_f32 v141, v88, v89
	s_addc_u32 s11, s11, 0
	v_mfma_f32_16x16x32_bf16 v[122:125], v[122:125], v[162:165], v[192:195]
	s_waitcnt lgkmcnt(7)
	v_pk_mul_f32 v[42:43], v[42:43], v[202:203]
	v_pk_mul_f32 v[40:41], v[40:41], v[200:201]
	s_waitcnt lgkmcnt(6)
	v_pk_mul_f32 v[62:63], v[62:63], v[206:207]
	v_mfma_f32_16x16x32_bf16 v[142:145], v[146:149], v[138:141], v[102:105]
	v_mul_f32_e64 v60, v60, v204
	v_mul_f32_e64 v61, v61, v205
	s_waitcnt lgkmcnt(5)
	v_pk_mul_f32 v[68:69], v[68:69], v[210:211]
	v_pk_mul_f32 v[66:67], v[66:67], v[208:209]
	v_lshl_add_u64 v[102:103], s[10:11], 0, v[100:101]
	v_lshl_add_u64 v[102:103], v[102:103], 0, v[64:65]
	global_load_dwordx2 v[94:95], v[102:103], off nt
	global_load_dwordx2 v[96:97], v[102:103], off offset:512 nt
	v_lshl_add_u64 v[102:103], s[10:11], 0, v[98:99]
	global_load_dwordx4 v[52:55], v[102:103], off nt
	v_mfma_f32_16x16x32_bf16 v[122:125], v[126:129], v[196:199], v[122:125]
	s_waitcnt lgkmcnt(4)
	v_pk_mul_f32 v[72:73], v[72:73], v[232:233]
	v_pk_mul_f32 v[70:71], v[70:71], v[230:231]
	s_waitcnt lgkmcnt(3)
	v_pk_mul_f32 v[76:77], v[76:77], v[236:237]
	v_mfma_f32_16x16x32_bf16 v[122:125], v[130:133], v[220:223], v[122:125]
	v_mul_f32_e64 v74, v74, v234
	v_mul_f32_e64 v75, v75, v235
	s_waitcnt lgkmcnt(2)
	v_pk_mul_f32 v[80:81], v[80:81], v[240:241]
	v_pk_mul_f32 v[78:79], v[78:79], v[238:239]
	v_mfma_f32_16x16x32_bf16 v[122:125], v[134:137], v[138:141], v[122:125]
	s_waitcnt lgkmcnt(1)
	v_pk_mul_f32 v[84:85], v[84:85], v[244:245]
	v_pk_mul_f32 v[82:83], v[82:83], v[242:243]
	s_waitcnt lgkmcnt(0)
	v_pk_mul_f32 v[88:89], v[88:89], v[248:249]
	v_pk_mul_f32 v[86:87], v[86:87], v[246:247]
	v_lshl_add_u64 v[128:129], v[112:113], 0, s[8:9]
	s_nop 0
	v_bfe_u32 v126, v122, 16, 1
	v_add3_u32 v122, v122, v126, s30
	v_lshl_add_u64 v[126:127], v[106:107], 0, s[8:9]
	global_store_short_d16_hi v[126:127], v122, off offset:-2048
	v_bfe_u32 v122, v142, 16, 1
	v_add3_u32 v122, v142, v122, s30
	s_nop 0
	v_mfma_f32_16x16x32_bf16 v[40:43], v[150:153], v[32:35], v[40:43]
	global_store_short_d16_hi v[128:129], v122, off
	v_bfe_u32 v122, v123, 16, 1
	v_add3_u32 v122, v123, v122, s30
	v_mfma_f32_16x16x32_bf16 v[60:63], v[154:157], v[32:35], v[60:63]
	global_store_short_d16_hi v[126:127], v122, off offset:-1024
	s_bitcmp1_b32 s18, 0
	s_cselect_b32 s10, 0x4a00, 0
	v_mfma_f32_16x16x32_bf16 v[66:69], v[158:161], v[32:35], v[66:69]
	s_and_b64 vcc, exec, s[38:39]
	v_mfma_f32_16x16x32_bf16 v[70:73], v[172:175], v[32:35], v[70:73]
	v_mfma_f32_16x16x32_bf16 v[74:77], v[176:179], v[32:35], v[74:77]
	v_mfma_f32_16x16x32_bf16 v[78:81], v[180:183], v[32:35], v[78:81]
	v_mfma_f32_16x16x32_bf16 v[82:85], v[184:187], v[32:35], v[82:85]
	v_mfma_f32_16x16x32_bf16 v[86:89], v[188:191], v[32:35], v[86:89]
	v_bfe_u32 v32, v143, 16, 1
	v_add3_u32 v34, v143, v32, s30
	v_lshl_add_u64 v[32:33], v[112:113], 0, s[8:9]
	global_store_short_d16_hi v[32:33], v34, off offset:1024
	v_bfe_u32 v32, v124, 16, 1
	v_add3_u32 v32, v124, v32, s30
	global_store_short_d16_hi v[126:127], v32, off
	v_bfe_u32 v32, v144, 16, 1
	v_add3_u32 v34, v144, v32, s30
	v_lshl_add_u64 v[32:33], v[112:113], 0, s[8:9]
	global_store_short_d16_hi v[32:33], v34, off offset:2048
	v_bfe_u32 v32, v125, 16, 1
	v_add3_u32 v32, v125, v32, s30
	global_store_short_d16_hi v[126:127], v32, off offset:1024
	v_bfe_u32 v32, v145, 16, 1
	v_add3_u32 v34, v145, v32, s30
	v_lshl_add_u64 v[32:33], v[112:113], 0, s[8:9]
	global_store_short_d16_hi v[32:33], v34, off offset:3072
	v_add_u32_e32 v32, s10, v120
	v_add_u32_e32 v33, s16, v32
	s_waitcnt vmcnt(37)
	s_cbranch_vccnz .Lh1_b1517
	ds_write_b128 v33, v[16:19]
	s_and_b64 vcc, exec, s[40:41]
	s_cbranch_vccz .Lh1_b1518

.Lh2_b1505:
	s_add_i32 s23, s18, -1
	s_min_u32 s10, s23, 60
	s_mul_i32 s10, s10, 0x8a00
	s_add_u32 s10, s4, s10
	s_addc_u32 s11, s5, 0
	s_add_u32 s12, s10, 0x19e00
	s_addc_u32 s13, s11, 0
	s_and_b64 vcc, exec, s[38:39]
	s_cbranch_vccnz .Lh2_b1509
	s_add_u32 s24, s12, s16
	s_addc_u32 s25, s13, s17
	v_lshl_add_u64 v[16:17], s[24:25], 0, v[98:99]
	global_load_dwordx4 v[16:19], v[16:17], off nt
	s_and_b64 vcc, exec, s[40:41]
	s_cbranch_vccz .Lh2_b1510

.Lh2_b1508:
	s_add_u32 s12, s12, s21
	s_addc_u32 s13, s13, s22
	v_lshl_add_u64 v[24:25], s[12:13], 0, v[98:99]
	global_load_dwordx4 v[24:27], v[24:25], off nt
	s_and_saveexec_b64 s[12:13], s[6:7]
	s_cbranch_execnz .Lh2_b1512
	s_branch .Lh2_b1513

.Lh2_b1510:
	s_add_u32 s24, s12, s19
	s_addc_u32 s25, s13, s20
	v_lshl_add_u64 v[20:21], s[24:25], 0, v[98:99]
	global_load_dwordx4 v[20:23], v[20:21], off nt
	s_and_b64 vcc, exec, s[42:43]
	s_cbranch_vccz .Lh2_b1508

.Lh2_b1512:
	v_lshl_add_u64 v[28:29], s[10:11], 0, v[98:99]
	v_add_co_u32_e32 v28, vcc, 0x22000, v28
	s_nop 1
	v_addc_co_u32_e32 v29, vcc, 0, v29, vcc
	global_load_dwordx4 v[28:31], v[28:29], off offset:1536 nt
.Lh2_b1513:
	s_or_b64 exec, exec, s[12:13]
	s_min_u32 s10, s23, 61
	s_mul_i32 s10, s10, 0x8a00
	s_add_u32 s10, s4, s10
	s_addc_u32 s11, s5, 0
	s_bitcmp1_b32 s23, 0
	s_cselect_b32 s12, 0x4a00, 0
	s_add_i32 s12, s12, 0
	v_add_u32_e32 v162, s12, v98
	ds_read_b128 v[122:125], v162
	ds_read_b128 v[126:129], v162 offset:1024
	ds_read_b128 v[130:133], v162 offset:2048
	ds_read_b128 v[134:137], v162 offset:3072
	ds_read_b128 v[116:119], v162 offset:4096
	ds_read_b128 v[138:141], v162 offset:5120
	ds_read_b128 v[142:145], v162 offset:6144
	ds_read_b128 v[146:149], v162 offset:7168
	ds_read_b128 v[150:153], v162 offset:8192
	ds_read_b128 v[154:157], v162 offset:9216
	ds_read_b128 v[158:161], v162 offset:10240
	ds_read_b128 v[172:175], v162 offset:11264
	ds_read_b128 v[176:179], v162 offset:12288
	ds_read_b128 v[180:183], v162 offset:13312
	ds_read_b128 v[184:187], v162 offset:14336
	ds_read_b128 v[188:191], v162 offset:15360
	ds_read_b128 v[192:195], v162 offset:16384
	ds_read_b128 v[196:199], v162 offset:17408
	v_add_u32_e32 v162, s12, v121
	ds_read_b128 v[200:203], v162 offset:18432
	ds_read_b128 v[204:207], v162 offset:18496
	ds_read_b128 v[208:211], v162 offset:18560
	ds_read_b128 v[230:233], v162 offset:18624
	ds_read_b128 v[234:237], v162 offset:18688
	ds_read_b128 v[238:241], v162 offset:18752
	ds_read_b128 v[242:245], v162 offset:18816
	ds_read_b128 v[246:249], v162 offset:18880
	s_waitcnt vmcnt(23) lgkmcnt(9)
	v_mfma_f32_16x16x32_bf16 v[192:195], v[192:195], v[36:39], 0
	v_cvt_pk_bf16_f32 v162, v40, v41
	v_cvt_pk_bf16_f32 v163, v42, v43
	v_cvt_pk_bf16_f32 v164, v60, v61
	s_waitcnt lgkmcnt(8)
	v_mfma_f32_16x16x32_bf16 v[36:39], v[196:199], v[36:39], 0
	v_cvt_pk_bf16_f32 v165, v62, v63
	v_cvt_pk_bf16_f32 v196, v66, v67
	v_cvt_pk_bf16_f32 v197, v68, v69
	v_mfma_f32_16x16x32_bf16 v[36:39], v[116:119], v[162:165], v[36:39]
	v_cvt_pk_bf16_f32 v198, v70, v71
	v_cvt_pk_bf16_f32 v199, v72, v73
	v_cvt_pk_bf16_f32 v220, v74, v75
	v_cvt_pk_bf16_f32 v221, v76, v77
	v_mfma_f32_16x16x32_bf16 v[36:39], v[138:141], v[196:199], v[36:39]
	v_cvt_pk_bf16_f32 v222, v78, v79
	v_cvt_pk_bf16_f32 v223, v80, v81
	s_add_u32 s10, s10, s14
	s_addc_u32 s11, s11, s15
	v_mfma_f32_16x16x32_bf16 v[36:39], v[142:145], v[220:223], v[36:39]
	s_add_u32 s10, s10, 0x11400
	v_cvt_pk_bf16_f32 v138, v82, v83
	v_cvt_pk_bf16_f32 v139, v84, v85
	v_cvt_pk_bf16_f32 v140, v86, v87
	v_cvt_pk_bf16_f32 v141, v88, v89
	s_addc_u32 s11, s11, 0
	v_mfma_f32_16x16x32_bf16 v[122:125], v[122:125], v[162:165], v[192:195]
	s_waitcnt lgkmcnt(7)
	v_pk_mul_f32 v[42:43], v[42:43], v[202:203]
	v_pk_mul_f32 v[40:41], v[40:41], v[200:201]
	s_waitcnt lgkmcnt(6)
	v_pk_mul_f32 v[62:63], v[62:63], v[206:207]
	v_mfma_f32_16x16x32_bf16 v[142:145], v[146:149], v[138:141], v[36:39]
	v_mul_f32_e64 v60, v60, v204
	v_mul_f32_e64 v61, v61, v205
	s_waitcnt lgkmcnt(5)
	v_pk_mul_f32 v[68:69], v[68:69], v[210:211]
	v_pk_mul_f32 v[66:67], v[66:67], v[208:209]
	v_lshl_add_u64 v[36:37], s[10:11], 0, v[100:101]
	v_lshl_add_u64 v[36:37], v[36:37], 0, v[64:65]
	global_load_dwordx2 v[102:103], v[36:37], off nt
	global_load_dwordx2 v[104:105], v[36:37], off offset:512 nt
	v_lshl_add_u64 v[36:37], s[10:11], 0, v[98:99]
	global_load_dwordx4 v[32:35], v[36:37], off nt
	v_mfma_f32_16x16x32_bf16 v[122:125], v[126:129], v[196:199], v[122:125]
	s_waitcnt lgkmcnt(4)
	v_pk_mul_f32 v[72:73], v[72:73], v[232:233]
	v_pk_mul_f32 v[70:71], v[70:71], v[230:231]
	s_waitcnt lgkmcnt(3)
	v_pk_mul_f32 v[76:77], v[76:77], v[236:237]
	v_mfma_f32_16x16x32_bf16 v[122:125], v[130:133], v[220:223], v[122:125]
	v_mul_f32_e64 v74, v74, v234
	v_mul_f32_e64 v75, v75, v235
	s_waitcnt lgkmcnt(2)
	v_pk_mul_f32 v[80:81], v[80:81], v[240:241]
	v_pk_mul_f32 v[78:79], v[78:79], v[238:239]
	v_mfma_f32_16x16x32_bf16 v[122:125], v[134:137], v[138:141], v[122:125]
	s_waitcnt lgkmcnt(1)
	v_pk_mul_f32 v[84:85], v[84:85], v[244:245]
	v_pk_mul_f32 v[82:83], v[82:83], v[242:243]
	s_waitcnt lgkmcnt(0)
	v_pk_mul_f32 v[88:89], v[88:89], v[248:249]
	v_pk_mul_f32 v[86:87], v[86:87], v[246:247]
	v_lshl_add_u64 v[128:129], v[112:113], 0, s[8:9]
	s_nop 0
	v_bfe_u32 v126, v122, 16, 1
	v_add3_u32 v122, v122, v126, s30
	v_lshl_add_u64 v[126:127], v[106:107], 0, s[8:9]
	global_store_short_d16_hi v[126:127], v122, off offset:-2048
	v_bfe_u32 v122, v142, 16, 1
	v_add3_u32 v122, v142, v122, s30
	s_nop 0
	v_mfma_f32_16x16x32_bf16 v[40:43], v[150:153], v[108:111], v[40:43]
	global_store_short_d16_hi v[128:129], v122, off
	v_bfe_u32 v122, v123, 16, 1
	v_add3_u32 v122, v123, v122, s30
	v_mfma_f32_16x16x32_bf16 v[60:63], v[154:157], v[108:111], v[60:63]
	global_store_short_d16_hi v[126:127], v122, off offset:-1024
	s_bitcmp1_b32 s18, 0
	s_cselect_b32 s10, 0x4a00, 0
	v_mfma_f32_16x16x32_bf16 v[66:69], v[158:161], v[108:111], v[66:69]
	s_and_b64 vcc, exec, s[38:39]
	v_mfma_f32_16x16x32_bf16 v[70:73], v[172:175], v[108:111], v[70:73]
	v_mfma_f32_16x16x32_bf16 v[74:77], v[176:179], v[108:111], v[74:77]
	v_mfma_f32_16x16x32_bf16 v[78:81], v[180:183], v[108:111], v[78:81]
	v_mfma_f32_16x16x32_bf16 v[82:85], v[184:187], v[108:111], v[82:85]
	v_mfma_f32_16x16x32_bf16 v[86:89], v[188:191], v[108:111], v[86:89]
	v_bfe_u32 v108, v143, 16, 1
	v_add3_u32 v110, v143, v108, s30
	v_lshl_add_u64 v[108:109], v[112:113], 0, s[8:9]
	global_store_short_d16_hi v[108:109], v110, off offset:1024
	v_bfe_u32 v108, v124, 16, 1
	v_add3_u32 v108, v124, v108, s30
	global_store_short_d16_hi v[126:127], v108, off
	v_bfe_u32 v108, v144, 16, 1
	v_add3_u32 v110, v144, v108, s30
	v_lshl_add_u64 v[108:109], v[112:113], 0, s[8:9]
	global_store_short_d16_hi v[108:109], v110, off offset:2048
	v_bfe_u32 v108, v125, 16, 1
	v_add3_u32 v108, v125, v108, s30
	global_store_short_d16_hi v[126:127], v108, off offset:1024
	v_bfe_u32 v108, v145, 16, 1
	v_add3_u32 v110, v145, v108, s30
	v_lshl_add_u64 v[108:109], v[112:113], 0, s[8:9]
	global_store_short_d16_hi v[108:109], v110, off offset:3072
	v_add_u32_e32 v108, s10, v120
	v_add_u32_e32 v109, s16, v108
	s_waitcnt vmcnt(37)
	s_cbranch_vccnz .Lh2_b1517
	ds_write_b128 v109, v[90:93]
	s_and_b64 vcc, exec, s[40:41]
	s_cbranch_vccz .Lh2_b1518

.LBB0_1522:
	s_lshl_b32 s14, s82, 10
	s_addk_i32 s14, 0x2000
	s_ashr_i32 s15, s14, 31
	s_add_u32 s14, s10, s14
	s_addc_u32 s15, s11, s15
	v_lshl_add_u64 v[20:21], s[14:15], 0, v[98:99]
	global_load_dwordx4 v[20:23], v[20:21], off nt
	s_and_b64 vcc, exec, s[42:43]
	s_cbranch_vccz .LBB0_1500
	s_branch .LBB0_1501

.LBB0_1621:
	v_mov_b64_e32 v[32:33], s[48:49]
	v_mad_u64_u32 v[32:33], s[6:7], v172, s1, v[32:33]
	v_mad_i32_i24 v33, v173, s1, v33
	v_lshlrev_b32_e32 v34, 1, v160
	v_mov_b32_e32 v35, v65
	v_lshl_add_u64 v[32:33], v[32:33], 0, v[34:35]
	v_add_co_u32_e32 v34, vcc, 0x48003000, v32
	v_mov_b32_e32 v127, 0
	s_nop 0
	v_addc_co_u32_e32 v35, vcc, 0, v33, vcc
	v_add_co_u32_e32 v36, vcc, 0x48008000, v32
	v_mov_b32_e32 v126, v127
	s_nop 0
	v_addc_co_u32_e32 v37, vcc, 0, v33, vcc
	v_add_co_u32_e32 v38, vcc, 0x4800e000, v32
	v_mov_b32_e32 v119, v127
	s_nop 0
	v_addc_co_u32_e32 v39, vcc, 0, v33, vcc
	v_add_co_u32_e32 v40, vcc, 0x48013000, v32
	v_mov_b32_e32 v118, v127
	s_nop 0
	v_addc_co_u32_e32 v41, vcc, 0, v33, vcc
	global_load_dwordx2 v[66:67], v[34:35], off offset:528 nt
	global_load_dwordx2 v[68:69], v[36:37], off offset:2576 nt
	global_load_dwordx2 v[70:71], v[38:39], off offset:528 nt
	global_load_dwordx2 v[72:73], v[40:41], off offset:2576 nt
	v_add_co_u32_e32 v34, vcc, 0x48019000, v32
	s_nop 1
	v_addc_co_u32_e32 v35, vcc, 0, v33, vcc
	v_add_co_u32_e32 v36, vcc, 0x4801e000, v32
	s_nop 1
	v_addc_co_u32_e32 v37, vcc, 0, v33, vcc
	v_add_co_u32_e32 v38, vcc, 0x48024000, v32
	s_nop 1
	v_addc_co_u32_e32 v39, vcc, 0, v33, vcc
	v_add_co_u32_e32 v32, vcc, 0x48029000, v32
	s_nop 1
	v_addc_co_u32_e32 v33, vcc, 0, v33, vcc
	global_load_dwordx2 v[74:75], v[34:35], off offset:528 nt
	global_load_dwordx2 v[76:77], v[36:37], off offset:2576 nt
	global_load_dwordx2 v[78:79], v[38:39], off offset:528 nt
	global_load_dwordx2 v[80:81], v[32:33], off offset:2576 nt
	v_lshl_add_u32 v32, v228, 4, 0
	v_cmp_lt_i32_e32 vcc, 0, v229
	ds_write_b128 v32, v[52:55]
	ds_write_b128 v32, v[48:51] offset:8192
	s_waitcnt lgkmcnt(0)
	s_barrier
	s_and_saveexec_b64 s[6:7], vcc
	s_cbranch_execz .LBB0_1631
	v_cmp_lt_u32_e32 vcc, 7, v229
	v_mov_b32_e32 v118, v65
	v_mov_b32_e32 v119, v65
	v_mov_b32_e32 v126, v65
	v_mov_b32_e32 v127, v65
	v_mov_b32_e32 v32, 0
	s_and_saveexec_b64 s[8:9], vcc
	s_cbranch_execz .LBB0_1626
	v_mov_b32_e32 v118, 0
	v_and_b32_e32 v32, 0x7ffffff8, v229
	v_lshl_add_u32 v33, v161, 4, 0
	s_mov_b32 s13, 0
	s_mov_b64 s[10:11], 0
	v_mov_b32_e32 v119, v118
	v_mov_b32_e32 v126, v118
	v_mov_b32_e32 v127, v118

.LBB0_1633:
	v_lshlrev_b32_e32 v128, 16, v138
	v_and_b32_e32 v129, 0xffff0000, v138
	s_waitcnt vmcnt(7)
	v_lshlrev_b32_e32 v64, 16, v66
	v_pk_fma_f32 v[128:129], v[0:1], v[118:119], v[128:129]
	v_mul_f32_e32 v119, 0x3d372713, v64
	v_mul_f32_e32 v119, v119, v64
	v_mul_f32_e32 v118, 0.5, v64
	v_fmac_f32_e32 v64, v119, v64
	v_mul_f32_e32 v64, 0x3f4c422a, v64
	v_add_f32_e32 v64, v64, v64
	v_mul_f32_e32 v64, 0x3fb8aa3b, v64
	v_exp_f32_e32 v64, v64
	v_lshlrev_b32_e32 v130, 16, v139
	v_and_b32_e32 v131, 0xffff0000, v139
	v_pk_fma_f32 v[130:131], v[2:3], v[126:127], v[130:131]
	v_add_f32_e32 v64, 1.0, v64
	v_rcp_f32_e32 v64, v64
	v_lshl_add_u64 v[122:123], s[48:49], 0, v[146:147]
	s_mov_b32 s6, 0x6e204000
	v_add_co_u32_e32 v32, vcc, s6, v122
	v_fma_f32 v64, v64, -2.0, 1.0
	v_add_f32_e32 v64, 1.0, v64
	v_mul_f32_e32 v64, v118, v64
	v_and_b32_e32 v118, 0xffff0000, v66
	v_mul_f32_e32 v126, 0x3d372713, v118
	v_mul_f32_e32 v126, v126, v118
	v_mul_f32_e32 v119, 0.5, v118
	v_fmac_f32_e32 v118, v126, v118
	v_mul_f32_e32 v118, 0x3f4c422a, v118
	v_add_f32_e32 v118, v118, v118
	v_mul_f32_e32 v118, 0x3fb8aa3b, v118
	v_exp_f32_e32 v118, v118
	v_addc_co_u32_e32 v33, vcc, 0, v123, vcc
	s_mov_b32 s6, 0x6e205000
	v_add_f32_e32 v118, 1.0, v118
	v_rcp_f32_e32 v118, v118
	v_add_co_u32_e32 v34, vcc, s6, v122
	v_lshl_add_u64 v[124:125], s[48:49], 0, v[150:151]
	v_fma_f32 v118, v118, -2.0, 1.0
	v_add_f32_e32 v118, 1.0, v118
	v_mul_f32_e32 v118, v119, v118
	v_lshlrev_b32_e32 v119, 16, v67
	v_mul_f32_e32 v127, 0x3d372713, v119
	v_mul_f32_e32 v127, v127, v119
	v_mul_f32_e32 v126, 0.5, v119
	v_fmac_f32_e32 v119, v127, v119
	v_mul_f32_e32 v119, 0x3f4c422a, v119
	v_add_f32_e32 v119, v119, v119
	v_mul_f32_e32 v119, 0x3fb8aa3b, v119
	v_exp_f32_e32 v119, v119
	v_addc_co_u32_e32 v35, vcc, 0, v123, vcc
	s_mov_b32 s6, 0x70202000
	v_add_f32_e32 v119, 1.0, v119
	v_rcp_f32_e32 v119, v119
	v_add_co_u32_e32 v36, vcc, s6, v124
	s_mov_b32 s6, 0x70203000
	v_fma_f32 v119, v119, -2.0, 1.0
	v_add_f32_e32 v119, 1.0, v119
	v_mul_f32_e32 v119, v126, v119
	v_and_b32_e32 v126, 0xffff0000, v67
	v_addc_co_u32_e32 v37, vcc, 0, v125, vcc
	v_mul_f32_e32 v132, 0x3d372713, v126
	v_add_co_u32_e32 v86, vcc, s6, v124
	v_mul_f32_e32 v132, v132, v126
	s_nop 0
	v_addc_co_u32_e32 v87, vcc, 0, v125, vcc
	s_mov_b32 s6, 0x6e206000
	v_mul_f32_e32 v127, 0.5, v126
	v_fmac_f32_e32 v126, v132, v126
	global_load_dwordx4 v[60:63], v[34:35], off offset:-4096 nt
	global_load_dwordx2 v[116:117], v[86:87], off offset:-4096 nt
	global_load_dwordx4 v[56:59], v[32:33], off offset:2048 nt
	global_load_dwordx2 v[112:113], v[36:37], off offset:1024 nt
	global_load_dwordx4 v[52:55], v[34:35], off nt
	global_load_dwordx2 v[108:109], v[36:37], off offset:2048 nt
	global_load_dwordx4 v[48:51], v[34:35], off offset:2048 nt
	global_load_dwordx2 v[104:105], v[36:37], off offset:3072 nt
	v_add_co_u32_e32 v32, vcc, s6, v122
	v_mul_f32_e32 v126, 0x3f4c422a, v126
	s_nop 0
	v_addc_co_u32_e32 v33, vcc, 0, v123, vcc
	s_mov_b32 s6, 0x6e207000
	v_add_f32_e32 v126, v126, v126
	v_add_co_u32_e32 v34, vcc, s6, v122
	v_mul_f32_e32 v126, 0x3fb8aa3b, v126
	s_nop 0
	v_addc_co_u32_e32 v35, vcc, 0, v123, vcc
	v_lshl_add_u64 v[120:121], s[48:49], 0, v[84:85]
	s_mov_b32 s6, 0x4802f000
	v_exp_f32_e32 v126, v126
	global_load_dwordx4 v[44:47], v[34:35], off offset:-4096 nt
	global_load_dwordx2 v[100:101], v[86:87], off nt
	global_load_dwordx4 v[40:43], v[32:33], off offset:2048 nt
	global_load_dwordx2 v[96:97], v[86:87], off offset:1024 nt
	global_load_dwordx4 v[36:39], v[34:35], off nt
	global_load_dwordx2 v[92:93], v[86:87], off offset:2048 nt
	s_nop 0
	global_load_dwordx4 v[32:35], v[34:35], off offset:2048 nt
	s_nop 0
	global_load_dwordx2 v[88:89], v[86:87], off offset:3072 nt
	v_add_co_u32_e32 v86, vcc, s6, v120
	s_mov_b32 s6, 0x48034000
	s_nop 0
	v_addc_co_u32_e32 v87, vcc, 0, v121, vcc
	global_load_dwordx2 v[114:115], v[86:87], off offset:528 nt
	v_add_co_u32_e32 v86, vcc, s6, v120
	s_mov_b32 s6, 0x4803a000
	s_nop 0
	v_addc_co_u32_e32 v87, vcc, 0, v121, vcc
	v_add_f32_e32 v126, 1.0, v126
	global_load_dwordx2 v[110:111], v[86:87], off offset:2576 nt
	v_add_co_u32_e32 v86, vcc, s6, v120
	v_rcp_f32_e32 v126, v126
	s_nop 0
	v_addc_co_u32_e32 v87, vcc, 0, v121, vcc
	s_mov_b32 s6, 0x4803f000
	global_load_dwordx2 v[106:107], v[86:87], off offset:528 nt
	v_add_co_u32_e32 v86, vcc, s6, v120
	s_mov_b32 s6, 0x48045000
	s_nop 0
	v_addc_co_u32_e32 v87, vcc, 0, v121, vcc
	v_mul_f32_e32 v64, v64, v128
	v_mul_f32_e32 v118, v118, v129
	global_load_dwordx2 v[102:103], v[86:87], off offset:2576 nt
	v_add_co_u32_e32 v86, vcc, s6, v120
	v_fma_f32 v126, v126, -2.0, 1.0
	v_mul_f32_e32 v64, 0x41000000, v64
	v_mul_f32_e32 v118, 0x41000000, v118
	v_addc_co_u32_e32 v87, vcc, 0, v121, vcc
	s_mov_b32 s6, 0x4804a000
	v_add_f32_e32 v126, 1.0, v126
	v_med3_f32 v64, v64, s3, v225
	v_med3_f32 v118, v118, s3, v225
	v_mov_b32_e32 v132, v65
	global_load_dwordx2 v[98:99], v[86:87], off offset:528 nt
	v_add_co_u32_e32 v86, vcc, s6, v120
	v_mul_f32_e32 v126, v127, v126
	v_cvt_pk_fp8_f32 v132, v64, v118
	v_addc_co_u32_e32 v87, vcc, 0, v121, vcc
	s_mov_b32 s6, 0x48050000
	v_mul_f32_e32 v119, v119, v130
	v_mul_f32_e32 v126, v126, v131
	global_load_dwordx2 v[94:95], v[86:87], off offset:2576 nt
	v_add_co_u32_e32 v86, vcc, s6, v120
	v_mul_f32_e32 v64, 0x41000000, v119
	v_mul_f32_e32 v118, 0x41000000, v126
	v_addc_co_u32_e32 v87, vcc, 0, v121, vcc
	s_mov_b32 s6, 0x48055000
	v_med3_f32 v64, v64, s3, v225
	v_med3_f32 v118, v118, s3, v225
	global_load_dwordx2 v[90:91], v[86:87], off offset:528 nt
	v_add_co_u32_e32 v86, vcc, s6, v120
	v_cvt_pk_fp8_f32 v132, v64, v118 op_sel:[0,0,1]
	s_nop 0
	v_addc_co_u32_e32 v87, vcc, 0, v121, vcc
	v_lshl_add_u64 v[118:119], s[48:49], 0, v[82:83]
	s_mov_b32 s6, 0x79a00000
	v_add_co_u32_e32 v126, vcc, s6, v118
	global_load_dwordx2 v[86:87], v[86:87], off offset:2576 nt
	s_nop 0
	v_addc_co_u32_e32 v127, vcc, 0, v119, vcc
	global_store_dword v[126:127], v132, off
	v_lshlrev_b32_e32 v132, 16, v140
	v_and_b32_e32 v133, 0xffff0000, v140
	s_waitcnt vmcnt(31)
	v_lshlrev_b32_e32 v64, 16, v68
	v_pk_fma_f32 v[128:129], v[4:5], v[128:129], v[132:133]
	v_mul_f32_e32 v133, 0x3d372713, v64
	v_mul_f32_e32 v133, v133, v64
	v_mul_f32_e32 v132, 0.5, v64
	v_fmac_f32_e32 v64, v133, v64
	v_mul_f32_e32 v64, 0x3f4c422a, v64
	v_add_f32_e32 v64, v64, v64
	v_mul_f32_e32 v64, 0x3fb8aa3b, v64
	v_exp_f32_e32 v64, v64
	v_lshlrev_b32_e32 v134, 16, v141
	v_and_b32_e32 v135, 0xffff0000, v141
	v_pk_fma_f32 v[130:131], v[6:7], v[130:131], v[134:135]
	v_add_f32_e32 v64, 1.0, v64
	v_rcp_f32_e32 v64, v64
	s_add_i32 s8, s8, 16
	s_cmp_gt_u32 s8, 47
	s_cselect_b64 s[6:7], -1, 0
	v_fma_f32 v64, v64, -2.0, 1.0
	v_add_f32_e32 v64, 1.0, v64
	v_mul_f32_e32 v64, v132, v64
	v_and_b32_e32 v132, 0xffff0000, v68
	v_mul_f32_e32 v134, 0x3d372713, v132
	v_mul_f32_e32 v134, v134, v132
	v_mul_f32_e32 v133, 0.5, v132
	v_fmac_f32_e32 v132, v134, v132
	v_mul_f32_e32 v132, 0x3f4c422a, v132
	v_add_f32_e32 v132, v132, v132
	v_mul_f32_e32 v132, 0x3fb8aa3b, v132
	v_exp_f32_e32 v132, v132
	v_mul_f32_e32 v64, v64, v128
	v_mul_f32_e32 v64, 0x41000000, v64
	v_med3_f32 v64, v64, s3, v225
	v_add_f32_e32 v132, 1.0, v132
	v_rcp_f32_e32 v132, v132
	s_and_b64 vcc, exec, s[6:7]
	v_fma_f32 v132, v132, -2.0, 1.0
	v_add_f32_e32 v132, 1.0, v132
	v_mul_f32_e32 v132, v133, v132
	v_lshlrev_b32_e32 v133, 16, v69
	v_mul_f32_e32 v135, 0x3d372713, v133
	v_mul_f32_e32 v135, v135, v133
	v_mul_f32_e32 v134, 0.5, v133
	v_fmac_f32_e32 v133, v135, v133
	v_mul_f32_e32 v133, 0x3f4c422a, v133
	v_add_f32_e32 v133, v133, v133
	v_mul_f32_e32 v133, 0x3fb8aa3b, v133
	v_exp_f32_e32 v133, v133
	v_mul_f32_e32 v132, v132, v129
	v_mul_f32_e32 v132, 0x41000000, v132
	v_med3_f32 v132, v132, s3, v225
	v_add_f32_e32 v133, 1.0, v133
	v_rcp_f32_e32 v133, v133
	s_nop 0
	v_fma_f32 v133, v133, -2.0, 1.0
	v_add_f32_e32 v133, 1.0, v133
	v_mul_f32_e32 v133, v134, v133
	v_and_b32_e32 v134, 0xffff0000, v69
	v_mul_f32_e32 v136, 0x3d372713, v134
	v_mul_f32_e32 v136, v136, v134
	v_mul_f32_e32 v135, 0.5, v134
	v_fmac_f32_e32 v134, v136, v134
	v_mul_f32_e32 v134, 0x3f4c422a, v134
	v_add_f32_e32 v134, v134, v134
	v_mul_f32_e32 v134, 0x3fb8aa3b, v134
	v_exp_f32_e32 v134, v134
	v_mul_f32_e32 v133, v133, v130
	v_add_f32_e32 v134, 1.0, v134
	v_rcp_f32_e32 v134, v134
	s_nop 0
	v_fma_f32 v134, v134, -2.0, 1.0
	v_add_f32_e32 v134, 1.0, v134
	v_mul_f32_e32 v134, v135, v134
	v_mov_b32_e32 v135, v65
	v_cvt_pk_fp8_f32 v135, v64, v132
	v_mul_f32_e32 v134, v134, v131
	v_mul_f32_e32 v64, 0x41000000, v133
	v_mul_f32_e32 v132, 0x41000000, v134
	v_med3_f32 v64, v64, s3, v225
	v_med3_f32 v132, v132, s3, v225
	v_cvt_pk_fp8_f32 v135, v64, v132 op_sel:[0,0,1]
	v_lshlrev_b32_e32 v132, 16, v142
	v_and_b32_e32 v133, 0xffff0000, v142
	s_waitcnt vmcnt(30)
	v_lshlrev_b32_e32 v64, 16, v70
	v_pk_fma_f32 v[128:129], v[8:9], v[128:129], v[132:133]
	v_mul_f32_e32 v133, 0x3d372713, v64
	v_mul_f32_e32 v133, v133, v64
	v_mul_f32_e32 v132, 0.5, v64
	v_fmac_f32_e32 v64, v133, v64
	v_mul_f32_e32 v64, 0x3f4c422a, v64
	v_add_f32_e32 v64, v64, v64
	v_mul_f32_e32 v64, 0x3fb8aa3b, v64
	v_exp_f32_e32 v64, v64
	global_store_dword v[126:127], v135, off offset:512
	v_lshlrev_b32_e32 v134, 16, v143
	v_and_b32_e32 v135, 0xffff0000, v143
	v_add_f32_e32 v64, 1.0, v64
	v_rcp_f32_e32 v64, v64
	v_pk_fma_f32 v[130:131], v[10:11], v[130:131], v[134:135]
	v_fma_f32 v64, v64, -2.0, 1.0
	v_add_f32_e32 v64, 1.0, v64
	v_mul_f32_e32 v64, v132, v64
	v_and_b32_e32 v132, 0xffff0000, v70
	v_mul_f32_e32 v134, 0x3d372713, v132
	v_mul_f32_e32 v134, v134, v132
	v_mul_f32_e32 v133, 0.5, v132
	v_fmac_f32_e32 v132, v134, v132
	v_mul_f32_e32 v132, 0x3f4c422a, v132
	v_add_f32_e32 v132, v132, v132
	v_mul_f32_e32 v132, 0x3fb8aa3b, v132
	v_exp_f32_e32 v132, v132
	v_mul_f32_e32 v64, v64, v128
	v_mul_f32_e32 v64, 0x41000000, v64
	v_med3_f32 v64, v64, s3, v225
	v_add_f32_e32 v132, 1.0, v132
	v_rcp_f32_e32 v132, v132
	s_nop 0
	v_fma_f32 v132, v132, -2.0, 1.0
	v_add_f32_e32 v132, 1.0, v132
	v_mul_f32_e32 v132, v133, v132
	v_lshlrev_b32_e32 v133, 16, v71
	v_mul_f32_e32 v135, 0x3d372713, v133
	v_mul_f32_e32 v135, v135, v133
	v_mul_f32_e32 v134, 0.5, v133
	v_fmac_f32_e32 v133, v135, v133
	v_mul_f32_e32 v133, 0x3f4c422a, v133
	v_add_f32_e32 v133, v133, v133
	v_mul_f32_e32 v133, 0x3fb8aa3b, v133
	v_exp_f32_e32 v133, v133
	v_mul_f32_e32 v132, v132, v129
	v_mul_f32_e32 v132, 0x41000000, v132
	v_med3_f32 v132, v132, s3, v225
	v_add_f32_e32 v133, 1.0, v133
	v_rcp_f32_e32 v133, v133
	s_nop 0
	v_fma_f32 v133, v133, -2.0, 1.0
	v_add_f32_e32 v133, 1.0, v133
	v_mul_f32_e32 v133, v134, v133
	v_and_b32_e32 v134, 0xffff0000, v71
	v_mul_f32_e32 v136, 0x3d372713, v134
	v_mul_f32_e32 v136, v136, v134
	v_mul_f32_e32 v135, 0.5, v134
	v_fmac_f32_e32 v134, v136, v134
	v_mul_f32_e32 v134, 0x3f4c422a, v134
	v_add_f32_e32 v134, v134, v134
	v_mul_f32_e32 v134, 0x3fb8aa3b, v134
	v_exp_f32_e32 v134, v134
	v_mul_f32_e32 v133, v133, v130
	v_add_f32_e32 v134, 1.0, v134
	v_rcp_f32_e32 v134, v134
	s_nop 0
	v_fma_f32 v134, v134, -2.0, 1.0
	v_add_f32_e32 v134, 1.0, v134
	v_mul_f32_e32 v134, v135, v134
	v_mov_b32_e32 v135, v65
	v_cvt_pk_fp8_f32 v135, v64, v132
	v_mul_f32_e32 v134, v134, v131
	v_mul_f32_e32 v64, 0x41000000, v133
	v_mul_f32_e32 v132, 0x41000000, v134
	v_med3_f32 v64, v64, s3, v225
	v_med3_f32 v132, v132, s3, v225
	v_cvt_pk_fp8_f32 v135, v64, v132 op_sel:[0,0,1]
	v_lshlrev_b32_e32 v132, 16, v144
	v_and_b32_e32 v133, 0xffff0000, v144
	s_waitcnt vmcnt(30)
	v_lshlrev_b32_e32 v64, 16, v72
	v_pk_fma_f32 v[128:129], v[12:13], v[128:129], v[132:133]
	v_mul_f32_e32 v133, 0x3d372713, v64
	v_mul_f32_e32 v133, v133, v64
	v_mul_f32_e32 v132, 0.5, v64
	v_fmac_f32_e32 v64, v133, v64
	v_mul_f32_e32 v64, 0x3f4c422a, v64
	v_add_f32_e32 v64, v64, v64
	v_mul_f32_e32 v64, 0x3fb8aa3b, v64
	v_exp_f32_e32 v64, v64
	global_store_dword v[126:127], v135, off offset:1024
	v_lshlrev_b32_e32 v134, 16, v145
	v_and_b32_e32 v135, 0xffff0000, v145
	v_add_f32_e32 v64, 1.0, v64
	v_rcp_f32_e32 v64, v64
	v_pk_fma_f32 v[130:131], v[14:15], v[130:131], v[134:135]
	v_fma_f32 v64, v64, -2.0, 1.0
	v_add_f32_e32 v64, 1.0, v64
	v_mul_f32_e32 v64, v132, v64
	v_and_b32_e32 v132, 0xffff0000, v72
	v_mul_f32_e32 v134, 0x3d372713, v132
	v_mul_f32_e32 v134, v134, v132
	v_mul_f32_e32 v133, 0.5, v132
	v_fmac_f32_e32 v132, v134, v132
	v_mul_f32_e32 v132, 0x3f4c422a, v132
	v_add_f32_e32 v132, v132, v132
	v_mul_f32_e32 v132, 0x3fb8aa3b, v132
	v_exp_f32_e32 v132, v132
	v_mul_f32_e32 v64, v64, v128
	v_mul_f32_e32 v64, 0x41000000, v64
	v_med3_f32 v64, v64, s3, v225
	v_add_f32_e32 v132, 1.0, v132
	v_rcp_f32_e32 v132, v132
	s_nop 0
	v_fma_f32 v132, v132, -2.0, 1.0
	v_add_f32_e32 v132, 1.0, v132
	v_mul_f32_e32 v132, v133, v132
	v_lshlrev_b32_e32 v133, 16, v73
	v_mul_f32_e32 v135, 0x3d372713, v133
	v_mul_f32_e32 v135, v135, v133
	v_mul_f32_e32 v134, 0.5, v133
	v_fmac_f32_e32 v133, v135, v133
	v_mul_f32_e32 v133, 0x3f4c422a, v133
	v_add_f32_e32 v133, v133, v133
	v_mul_f32_e32 v133, 0x3fb8aa3b, v133
	v_exp_f32_e32 v133, v133
	v_mul_f32_e32 v132, v132, v129
	v_mul_f32_e32 v132, 0x41000000, v132
	v_med3_f32 v132, v132, s3, v225
	v_add_f32_e32 v133, 1.0, v133
	v_rcp_f32_e32 v133, v133
	s_nop 0
	v_fma_f32 v133, v133, -2.0, 1.0
	v_add_f32_e32 v133, 1.0, v133
	v_mul_f32_e32 v133, v134, v133
	v_and_b32_e32 v134, 0xffff0000, v73
	v_mul_f32_e32 v136, 0x3d372713, v134
	v_mul_f32_e32 v136, v136, v134
	v_mul_f32_e32 v135, 0.5, v134
	v_fmac_f32_e32 v134, v136, v134
	v_mul_f32_e32 v134, 0x3f4c422a, v134
	v_add_f32_e32 v134, v134, v134
	v_mul_f32_e32 v134, 0x3fb8aa3b, v134
	v_exp_f32_e32 v134, v134
	v_mul_f32_e32 v133, v133, v130
	v_add_f32_e32 v134, 1.0, v134
	v_rcp_f32_e32 v134, v134
	s_nop 0
	v_fma_f32 v134, v134, -2.0, 1.0
	v_add_f32_e32 v134, 1.0, v134
	v_mul_f32_e32 v134, v135, v134
	v_mov_b32_e32 v135, v65
	v_cvt_pk_fp8_f32 v135, v64, v132
	v_mul_f32_e32 v134, v134, v131
	v_mul_f32_e32 v64, 0x41000000, v133
	v_mul_f32_e32 v132, 0x41000000, v134
	v_med3_f32 v64, v64, s3, v225
	v_med3_f32 v132, v132, s3, v225
	v_cvt_pk_fp8_f32 v135, v64, v132 op_sel:[0,0,1]
	v_lshlrev_b32_e32 v132, 16, v148
	v_and_b32_e32 v133, 0xffff0000, v148
	s_waitcnt vmcnt(30)
	v_lshlrev_b32_e32 v64, 16, v74
	v_pk_fma_f32 v[128:129], v[16:17], v[128:129], v[132:133]
	v_mul_f32_e32 v133, 0x3d372713, v64
	v_mul_f32_e32 v133, v133, v64
	v_mul_f32_e32 v132, 0.5, v64
	v_fmac_f32_e32 v64, v133, v64
	v_mul_f32_e32 v64, 0x3f4c422a, v64
	v_add_f32_e32 v64, v64, v64
	v_mul_f32_e32 v64, 0x3fb8aa3b, v64
	v_exp_f32_e32 v64, v64
	global_store_dword v[126:127], v135, off offset:1536
	v_lshlrev_b32_e32 v134, 16, v149
	v_and_b32_e32 v135, 0xffff0000, v149
	v_add_f32_e32 v64, 1.0, v64
	v_rcp_f32_e32 v64, v64
	v_pk_fma_f32 v[130:131], v[18:19], v[130:131], v[134:135]
	v_fma_f32 v64, v64, -2.0, 1.0
	v_add_f32_e32 v64, 1.0, v64
	v_mul_f32_e32 v64, v132, v64
	v_and_b32_e32 v132, 0xffff0000, v74
	v_mul_f32_e32 v134, 0x3d372713, v132
	v_mul_f32_e32 v134, v134, v132
	v_mul_f32_e32 v133, 0.5, v132
	v_fmac_f32_e32 v132, v134, v132
	v_mul_f32_e32 v132, 0x3f4c422a, v132
	v_add_f32_e32 v132, v132, v132
	v_mul_f32_e32 v132, 0x3fb8aa3b, v132
	v_exp_f32_e32 v132, v132
	v_mul_f32_e32 v64, v64, v128
	v_mul_f32_e32 v64, 0x41000000, v64
	v_med3_f32 v64, v64, s3, v225
	v_add_f32_e32 v132, 1.0, v132
	v_rcp_f32_e32 v132, v132
	s_nop 0
	v_fma_f32 v132, v132, -2.0, 1.0
	v_add_f32_e32 v132, 1.0, v132
	v_mul_f32_e32 v132, v133, v132
	v_lshlrev_b32_e32 v133, 16, v75
	v_mul_f32_e32 v135, 0x3d372713, v133
	v_mul_f32_e32 v135, v135, v133
	v_mul_f32_e32 v134, 0.5, v133
	v_fmac_f32_e32 v133, v135, v133
	v_mul_f32_e32 v133, 0x3f4c422a, v133
	v_add_f32_e32 v133, v133, v133
	v_mul_f32_e32 v133, 0x3fb8aa3b, v133
	v_exp_f32_e32 v133, v133
	v_mul_f32_e32 v132, v132, v129
	v_mul_f32_e32 v132, 0x41000000, v132
	v_med3_f32 v132, v132, s3, v225
	v_add_f32_e32 v133, 1.0, v133
	v_rcp_f32_e32 v133, v133
	s_nop 0
	v_fma_f32 v133, v133, -2.0, 1.0
	v_add_f32_e32 v133, 1.0, v133
	v_mul_f32_e32 v133, v134, v133
	v_and_b32_e32 v134, 0xffff0000, v75
	v_mul_f32_e32 v136, 0x3d372713, v134
	v_mul_f32_e32 v136, v136, v134
	v_mul_f32_e32 v135, 0.5, v134
	v_fmac_f32_e32 v134, v136, v134
	v_mul_f32_e32 v134, 0x3f4c422a, v134
	v_add_f32_e32 v134, v134, v134
	v_mul_f32_e32 v134, 0x3fb8aa3b, v134
	v_exp_f32_e32 v134, v134
	v_mul_f32_e32 v133, v133, v130
	v_add_f32_e32 v134, 1.0, v134
	v_rcp_f32_e32 v134, v134
	s_nop 0
	v_fma_f32 v134, v134, -2.0, 1.0
	v_add_f32_e32 v134, 1.0, v134
	v_mul_f32_e32 v134, v135, v134
	v_mov_b32_e32 v135, v65
	v_cvt_pk_fp8_f32 v135, v64, v132
	v_mul_f32_e32 v134, v134, v131
	v_mul_f32_e32 v64, 0x41000000, v133
	v_mul_f32_e32 v132, 0x41000000, v134
	v_med3_f32 v64, v64, s3, v225
	v_med3_f32 v132, v132, s3, v225
	v_cvt_pk_fp8_f32 v135, v64, v132 op_sel:[0,0,1]
	v_lshlrev_b32_e32 v132, 16, v152
	v_and_b32_e32 v133, 0xffff0000, v152
	s_waitcnt vmcnt(30)
	v_lshlrev_b32_e32 v64, 16, v76
	v_pk_fma_f32 v[128:129], v[20:21], v[128:129], v[132:133]
	v_mul_f32_e32 v133, 0x3d372713, v64
	v_mul_f32_e32 v133, v133, v64
	v_mul_f32_e32 v132, 0.5, v64
	v_fmac_f32_e32 v64, v133, v64
	v_mul_f32_e32 v64, 0x3f4c422a, v64
	v_add_f32_e32 v64, v64, v64
	v_mul_f32_e32 v64, 0x3fb8aa3b, v64
	v_exp_f32_e32 v64, v64
	global_store_dword v[126:127], v135, off offset:2048
	v_lshlrev_b32_e32 v134, 16, v153
	v_and_b32_e32 v135, 0xffff0000, v153
	v_add_f32_e32 v64, 1.0, v64
	v_rcp_f32_e32 v64, v64
	v_pk_fma_f32 v[130:131], v[22:23], v[130:131], v[134:135]
	v_fma_f32 v64, v64, -2.0, 1.0
	v_add_f32_e32 v64, 1.0, v64
	v_mul_f32_e32 v64, v132, v64
	v_and_b32_e32 v132, 0xffff0000, v76
	v_mul_f32_e32 v134, 0x3d372713, v132
	v_mul_f32_e32 v134, v134, v132
	v_mul_f32_e32 v133, 0.5, v132
	v_fmac_f32_e32 v132, v134, v132
	v_mul_f32_e32 v132, 0x3f4c422a, v132
	v_add_f32_e32 v132, v132, v132
	v_mul_f32_e32 v132, 0x3fb8aa3b, v132
	v_exp_f32_e32 v132, v132
	v_mul_f32_e32 v64, v64, v128
	v_mul_f32_e32 v64, 0x41000000, v64
	v_med3_f32 v64, v64, s3, v225
	v_add_f32_e32 v132, 1.0, v132
	v_rcp_f32_e32 v132, v132
	s_nop 0
	v_fma_f32 v132, v132, -2.0, 1.0
	v_add_f32_e32 v132, 1.0, v132
	v_mul_f32_e32 v132, v133, v132
	v_lshlrev_b32_e32 v133, 16, v77
	v_mul_f32_e32 v135, 0x3d372713, v133
	v_mul_f32_e32 v135, v135, v133
	v_mul_f32_e32 v134, 0.5, v133
	v_fmac_f32_e32 v133, v135, v133
	v_mul_f32_e32 v133, 0x3f4c422a, v133
	v_add_f32_e32 v133, v133, v133
	v_mul_f32_e32 v133, 0x3fb8aa3b, v133
	v_exp_f32_e32 v133, v133
	v_mul_f32_e32 v132, v132, v129
	v_mul_f32_e32 v132, 0x41000000, v132
	v_med3_f32 v132, v132, s3, v225
	v_add_f32_e32 v133, 1.0, v133
	v_rcp_f32_e32 v133, v133
	s_nop 0
	v_fma_f32 v133, v133, -2.0, 1.0
	v_add_f32_e32 v133, 1.0, v133
	v_mul_f32_e32 v133, v134, v133
	v_and_b32_e32 v134, 0xffff0000, v77
	v_mul_f32_e32 v136, 0x3d372713, v134
	v_mul_f32_e32 v136, v136, v134
	v_mul_f32_e32 v135, 0.5, v134
	v_fmac_f32_e32 v134, v136, v134
	v_mul_f32_e32 v134, 0x3f4c422a, v134
	v_add_f32_e32 v134, v134, v134
	v_mul_f32_e32 v134, 0x3fb8aa3b, v134
	v_exp_f32_e32 v134, v134
	v_mul_f32_e32 v133, v133, v130
	v_add_f32_e32 v134, 1.0, v134
	v_rcp_f32_e32 v134, v134
	s_nop 0
	v_fma_f32 v134, v134, -2.0, 1.0
	v_add_f32_e32 v134, 1.0, v134
	v_mul_f32_e32 v134, v135, v134
	v_mov_b32_e32 v135, v65
	v_cvt_pk_fp8_f32 v135, v64, v132
	v_mul_f32_e32 v134, v134, v131
	v_mul_f32_e32 v64, 0x41000000, v133
	v_mul_f32_e32 v132, 0x41000000, v134
	v_med3_f32 v64, v64, s3, v225
	v_med3_f32 v132, v132, s3, v225
	v_cvt_pk_fp8_f32 v135, v64, v132 op_sel:[0,0,1]
	v_lshlrev_b32_e32 v132, 16, v154
	v_and_b32_e32 v133, 0xffff0000, v154
	s_waitcnt vmcnt(30)
	v_lshlrev_b32_e32 v64, 16, v78
	v_pk_fma_f32 v[132:133], v[24:25], v[128:129], v[132:133]
	v_mul_f32_e32 v129, 0x3d372713, v64
	v_mul_f32_e32 v129, v129, v64
	v_mul_f32_e32 v128, 0.5, v64
	v_fmac_f32_e32 v64, v129, v64
	v_mul_f32_e32 v64, 0x3f4c422a, v64
	v_add_f32_e32 v64, v64, v64
	v_mul_f32_e32 v64, 0x3fb8aa3b, v64
	v_exp_f32_e32 v64, v64
	global_store_dword v[126:127], v135, off offset:2560
	v_lshlrev_b32_e32 v134, 16, v155
	v_and_b32_e32 v135, 0xffff0000, v155
	v_add_f32_e32 v64, 1.0, v64
	v_rcp_f32_e32 v64, v64
	v_pk_fma_f32 v[130:131], v[26:27], v[130:131], v[134:135]
	v_fma_f32 v64, v64, -2.0, 1.0
	v_add_f32_e32 v64, 1.0, v64
	v_mul_f32_e32 v64, v128, v64
	v_and_b32_e32 v128, 0xffff0000, v78
	v_mul_f32_e32 v134, 0x3d372713, v128
	v_mul_f32_e32 v134, v134, v128
	v_mul_f32_e32 v129, 0.5, v128
	v_fmac_f32_e32 v128, v134, v128
	v_mul_f32_e32 v128, 0x3f4c422a, v128
	v_add_f32_e32 v128, v128, v128
	v_mul_f32_e32 v128, 0x3fb8aa3b, v128
	v_exp_f32_e32 v128, v128
	v_mul_f32_e32 v64, v64, v132
	v_mul_f32_e32 v64, 0x41000000, v64
	v_med3_f32 v64, v64, s3, v225
	v_add_f32_e32 v128, 1.0, v128
	v_rcp_f32_e32 v128, v128
	s_nop 0
	v_fma_f32 v128, v128, -2.0, 1.0
	v_add_f32_e32 v128, 1.0, v128
	v_mul_f32_e32 v128, v129, v128
	v_lshlrev_b32_e32 v129, 16, v79
	v_mul_f32_e32 v135, 0x3d372713, v129
	v_mul_f32_e32 v135, v135, v129
	v_mul_f32_e32 v134, 0.5, v129
	v_fmac_f32_e32 v129, v135, v129
	v_mul_f32_e32 v129, 0x3f4c422a, v129
	v_add_f32_e32 v129, v129, v129
	v_mul_f32_e32 v129, 0x3fb8aa3b, v129
	v_exp_f32_e32 v129, v129
	v_mul_f32_e32 v128, v128, v133
	v_mul_f32_e32 v128, 0x41000000, v128
	v_med3_f32 v128, v128, s3, v225
	v_add_f32_e32 v129, 1.0, v129
	v_rcp_f32_e32 v129, v129
	s_nop 0
	v_fma_f32 v129, v129, -2.0, 1.0
	v_add_f32_e32 v129, 1.0, v129
	v_mul_f32_e32 v129, v134, v129
	v_and_b32_e32 v134, 0xffff0000, v79
	v_mul_f32_e32 v136, 0x3d372713, v134
	v_mul_f32_e32 v136, v136, v134
	v_mul_f32_e32 v135, 0.5, v134
	v_fmac_f32_e32 v134, v136, v134
	v_mul_f32_e32 v134, 0x3f4c422a, v134
	v_add_f32_e32 v134, v134, v134
	v_mul_f32_e32 v134, 0x3fb8aa3b, v134
	v_exp_f32_e32 v134, v134
	v_mul_f32_e32 v129, v129, v130
	v_add_f32_e32 v134, 1.0, v134
	v_rcp_f32_e32 v134, v134
	s_nop 0
	v_fma_f32 v134, v134, -2.0, 1.0
	v_add_f32_e32 v134, 1.0, v134
	v_mul_f32_e32 v134, v135, v134
	v_mov_b32_e32 v135, v65
	v_cvt_pk_fp8_f32 v135, v64, v128
	v_mul_f32_e32 v134, v134, v131
	v_mul_f32_e32 v64, 0x41000000, v129
	v_mul_f32_e32 v128, 0x41000000, v134
	v_med3_f32 v64, v64, s3, v225
	v_med3_f32 v128, v128, s3, v225
	v_cvt_pk_fp8_f32 v135, v64, v128 op_sel:[0,0,1]
	v_lshlrev_b32_e32 v134, 16, v156
	v_lshlrev_b32_e32 v128, 16, v157
	v_and_b32_e32 v129, 0xffff0000, v157
	global_store_dword v[126:127], v135, off offset:3072
	v_and_b32_e32 v135, 0xffff0000, v156
	s_waitcnt vmcnt(31)
	v_lshlrev_b32_e32 v64, 16, v80
	v_pk_fma_f32 v[128:129], v[30:31], v[130:131], v[128:129]
	v_pk_fma_f32 v[130:131], v[28:29], v[132:133], v[134:135]
	v_mul_f32_e32 v133, 0x3d372713, v64
	v_mul_f32_e32 v133, v133, v64
	v_mul_f32_e32 v132, 0.5, v64
	v_fmac_f32_e32 v64, v133, v64
	v_mul_f32_e32 v64, 0x3f4c422a, v64
	v_add_f32_e32 v64, v64, v64
	v_mul_f32_e32 v64, 0x3fb8aa3b, v64
	v_exp_f32_e32 v64, v64
	s_nop 0
	v_add_f32_e32 v64, 1.0, v64
	v_rcp_f32_e32 v64, v64
	s_nop 0
	v_fma_f32 v64, v64, -2.0, 1.0
	v_add_f32_e32 v64, 1.0, v64
	v_mul_f32_e32 v64, v132, v64
	v_and_b32_e32 v132, 0xffff0000, v80
	v_mul_f32_e32 v134, 0x3d372713, v132
	v_mul_f32_e32 v134, v134, v132
	v_mul_f32_e32 v133, 0.5, v132
	v_fmac_f32_e32 v132, v134, v132
	v_mul_f32_e32 v132, 0x3f4c422a, v132
	v_add_f32_e32 v132, v132, v132
	v_mul_f32_e32 v132, 0x3fb8aa3b, v132
	v_exp_f32_e32 v132, v132
	v_mul_f32_e32 v64, v64, v130
	v_mul_f32_e32 v64, 0x41000000, v64
	v_med3_f32 v64, v64, s3, v225
	v_add_f32_e32 v132, 1.0, v132
	v_rcp_f32_e32 v132, v132
	s_nop 0
	v_fma_f32 v132, v132, -2.0, 1.0
	v_add_f32_e32 v132, 1.0, v132
	v_mul_f32_e32 v132, v133, v132
	v_lshlrev_b32_e32 v133, 16, v81
	v_mul_f32_e32 v135, 0x3d372713, v133
	v_mul_f32_e32 v135, v135, v133
	v_mul_f32_e32 v134, 0.5, v133
	v_fmac_f32_e32 v133, v135, v133
	v_mul_f32_e32 v133, 0x3f4c422a, v133
	v_add_f32_e32 v133, v133, v133
	v_mul_f32_e32 v133, 0x3fb8aa3b, v133
	v_exp_f32_e32 v133, v133
	v_mul_f32_e32 v132, v132, v131
	v_mul_f32_e32 v132, 0x41000000, v132
	v_med3_f32 v132, v132, s3, v225
	v_add_f32_e32 v133, 1.0, v133
	v_rcp_f32_e32 v133, v133
	s_nop 0
	v_fma_f32 v133, v133, -2.0, 1.0
	v_add_f32_e32 v133, 1.0, v133
	v_mul_f32_e32 v133, v134, v133
	v_and_b32_e32 v134, 0xffff0000, v81
	v_mul_f32_e32 v136, 0x3d372713, v134
	v_mul_f32_e32 v136, v136, v134
	v_mul_f32_e32 v135, 0.5, v134
	v_fmac_f32_e32 v134, v136, v134
	v_mul_f32_e32 v134, 0x3f4c422a, v134
	v_add_f32_e32 v134, v134, v134
	v_mul_f32_e32 v134, 0x3fb8aa3b, v134
	v_exp_f32_e32 v134, v134
	v_mul_f32_e32 v133, v133, v128
	v_add_f32_e32 v134, 1.0, v134
	v_rcp_f32_e32 v134, v134
	s_nop 0
	v_fma_f32 v134, v134, -2.0, 1.0
	v_add_f32_e32 v134, 1.0, v134
	v_mul_f32_e32 v134, v135, v134
	v_mov_b32_e32 v135, v65
	v_cvt_pk_fp8_f32 v135, v64, v132
	v_mul_f32_e32 v134, v134, v129
	v_mul_f32_e32 v64, 0x41000000, v133
	v_mul_f32_e32 v132, 0x41000000, v134
	v_med3_f32 v64, v64, s3, v225
	v_med3_f32 v132, v132, s3, v225
	v_cvt_pk_fp8_f32 v135, v64, v132 op_sel:[0,0,1]
	global_store_dword v[126:127], v135, off offset:3584
	s_cbranch_vccnz .LBB0_1632
	v_add_co_u32_e32 v4, vcc, 0x6e208000, v122
	s_nop 1
	v_addc_co_u32_e32 v5, vcc, 0, v123, vcc
	v_add_co_u32_e32 v16, vcc, 0x70204000, v124
	global_load_dwordx4 v[0:3], v[4:5], off nt
	s_nop 0
	global_load_dwordx4 v[4:7], v[4:5], off offset:2048 nt
	v_addc_co_u32_e32 v17, vcc, 0, v125, vcc
	v_add_co_u32_e32 v12, vcc, 0x6e209000, v122
	s_nop 1
	v_addc_co_u32_e32 v13, vcc, 0, v123, vcc
	v_add_co_u32_e32 v20, vcc, 0x6e20a000, v122
	global_load_dwordx4 v[8:11], v[12:13], off nt
	s_nop 0
	global_load_dwordx4 v[12:15], v[12:13], off offset:2048 nt
	s_nop 0
	global_load_dwordx2 v[138:139], v[16:17], off nt
	global_load_dwordx2 v[140:141], v[16:17], off offset:1024 nt
	global_load_dwordx2 v[142:143], v[16:17], off offset:2048 nt
	global_load_dwordx2 v[144:145], v[16:17], off offset:3072 nt
	v_addc_co_u32_e32 v21, vcc, 0, v123, vcc
	v_add_co_u32_e32 v66, vcc, 0x70205000, v124
	global_load_dwordx4 v[16:19], v[20:21], off nt
	s_nop 0
	global_load_dwordx4 v[20:23], v[20:21], off offset:2048 nt
	v_addc_co_u32_e32 v67, vcc, 0, v125, vcc
	v_add_co_u32_e32 v28, vcc, 0x6e20b000, v122
	s_nop 1
	v_addc_co_u32_e32 v29, vcc, 0, v123, vcc
	global_load_dwordx4 v[24:27], v[28:29], off nt
	s_nop 0
	global_load_dwordx4 v[28:31], v[28:29], off offset:2048 nt
	s_nop 0
	global_load_dwordx2 v[148:149], v[66:67], off nt
	global_load_dwordx2 v[152:153], v[66:67], off offset:1024 nt
	global_load_dwordx2 v[154:155], v[66:67], off offset:2048 nt
	global_load_dwordx2 v[156:157], v[66:67], off offset:3072 nt
	v_add_co_u32_e32 v66, vcc, 0x4805b000, v120
	s_nop 1
	v_addc_co_u32_e32 v67, vcc, 0, v121, vcc
	v_add_co_u32_e32 v68, vcc, 0x48060000, v120
	s_nop 1
	v_addc_co_u32_e32 v69, vcc, 0, v121, vcc
	v_add_co_u32_e32 v70, vcc, 0x48066000, v120
	s_nop 1
	v_addc_co_u32_e32 v71, vcc, 0, v121, vcc
	v_add_co_u32_e32 v72, vcc, 0x4806b000, v120
	s_nop 1
	v_addc_co_u32_e32 v73, vcc, 0, v121, vcc
	v_add_co_u32_e32 v74, vcc, 0x48071000, v120
	global_load_dwordx2 v[66:67], v[66:67], off offset:528 nt
	s_nop 0
	global_load_dwordx2 v[68:69], v[68:69], off offset:2576 nt
	s_nop 0
	global_load_dwordx2 v[70:71], v[70:71], off offset:528 nt
	s_nop 0
	global_load_dwordx2 v[72:73], v[72:73], off offset:2576 nt
	v_addc_co_u32_e32 v75, vcc, 0, v121, vcc
	v_add_co_u32_e32 v76, vcc, 0x48076000, v120
	s_nop 1
	v_addc_co_u32_e32 v77, vcc, 0, v121, vcc
	v_add_co_u32_e32 v78, vcc, 0x4807c000, v120
	s_nop 1
	v_addc_co_u32_e32 v79, vcc, 0, v121, vcc
	v_add_co_u32_e32 v80, vcc, 0x48081000, v120
	s_nop 1
	v_addc_co_u32_e32 v81, vcc, 0, v121, vcc
	global_load_dwordx2 v[74:75], v[74:75], off offset:528 nt
	s_nop 0
	global_load_dwordx2 v[76:77], v[76:77], off offset:2576 nt
	s_nop 0
	global_load_dwordx2 v[78:79], v[78:79], off offset:528 nt
	s_nop 0
	global_load_dwordx2 v[80:81], v[80:81], off offset:2576 nt
	s_branch .LBB0_1632
